# gemm_stagger_barrier_moved_after_next_unit_scheduling_math
# baseline (speedup 1.0000x reference)
_Z6mk_fwd4Args:
	s_mov_b32 s101, 0
	s_load_dword s10, s[0:1], 0x90
	s_mov_b32 s11, s2
	s_add_u32 s2, s0, 0x90
	s_addc_u32 s3, s1, 0
	v_lshl_add_u32 v1, v0, 2, 0
	v_writelane_b32 v253, s2, 0
	v_add_u32_e32 v1, 0x20000, v1
	v_mov_b32_e32 v2, 0
	v_readfirstlane_b32 s22, v0
	v_writelane_b32 v253, s3, 1
	ds_write2st64_b32 v1, v2, v2 offset1:8
	ds_write2st64_b32 v1, v2, v2 offset0:16 offset1:24
	v_or_b32_e32 v1, 0x800, v0
	s_mov_b64 s[2:3], -1
	s_and_saveexec_b64 s[4:5], s[2:3]
	v_lshl_add_u32 v3, v1, 2, 0
	v_add_u32_e32 v3, 0x20000, v3
	ds_write_b32 v3, v2
	s_or_b64 exec, exec, s[4:5]
	s_and_saveexec_b64 s[4:5], s[2:3]
	s_add_i32 s2, 0, 0x20000
	v_lshl_add_u32 v1, v1, 2, s2
	v_mov_b32_e32 v2, 0
	ds_write_b32 v1, v2 offset:2048
	s_or_b64 exec, exec, s[4:5]
	v_or_b32_e32 v1, 0xc00, v0
	v_cmp_gt_u32_e64 s[2:3], 7, 6
	v_cmp_gt_u32_e64 s[6:7], 7, 5
	s_and_saveexec_b64 s[4:5], s[6:7]
	v_lshl_add_u32 v2, v1, 2, 0
	v_add_u32_e32 v2, 0x20000, v2
	v_mov_b32_e32 v3, 0
	ds_write_b32 v2, v3
	s_or_b64 exec, exec, s[4:5]
	s_load_dwordx16 s[48:63], s[0:1], 0x40
	s_and_saveexec_b64 s[4:5], s[2:3]
	s_add_i32 s2, 0, 0x20000
	v_lshl_add_u32 v1, v1, 2, s2
	v_mov_b32_e32 v2, 0
	ds_write_b32 v1, v2 offset:2048
	s_or_b64 exec, exec, s[4:5]
	s_waitcnt lgkmcnt(0)
	s_add_u32 s2, s62, 0x4000
	s_addc_u32 s3, s63, 0
	v_writelane_b32 v253, s2, 2
	s_barrier
	s_nop 0
	v_writelane_b32 v253, s3, 3
	s_getreg_b32 s6, hwreg(HW_REG_XCC_ID, 0, 4)
	v_cmp_eq_u32_e64 s[4:5], 0, v0
	s_mov_b64 s[2:3], exec
	s_nop 0
	v_writelane_b32 v253, s4, 4
	s_nop 1
	v_writelane_b32 v253, s5, 5
	s_and_b64 s[4:5], s[2:3], s[4:5]
	s_mov_b64 exec, s[4:5]
	s_cbranch_execz .LBB0_11
	s_mov_b64 s[4:5], exec
	v_mbcnt_lo_u32_b32 v1, s4, 0
	v_mbcnt_hi_u32_b32 v1, s5, v1
	v_cmp_eq_u32_e32 vcc, 0, v1
	s_and_b64 s[8:9], exec, vcc
	s_mov_b64 exec, s[8:9]
	s_cbranch_execz .LBB0_11
	s_lshl_b32 s6, s6, 8
	s_bcnt1_i32_b64 s4, s[4:5]
	s_and_b32 s6, s6, 0xf00
	v_mov_b32_e32 v2, s4
	v_readlane_b32 s4, v253, 2
	v_mov_b32_e32 v1, s6
	v_readlane_b32 s5, v253, 3
	s_nop 4
	global_atomic_add v1, v2, s[4:5] offset:1024

.LBB0_251:
	s_mov_b64 s[26:27], 0
	s_add_u32 s0, s0, s26
	s_addc_u32 s1, s1, s27
	s_add_u32 s4, s4, s26
	s_addc_u32 s5, s5, s27
	s_mov_b32 s25, 16
	s_cmp_lt_i32 s25, 1
	s_cbranch_scc1 .LBB0_267
	s_ashr_i32 s23, s22, 31
	s_lshl_b64 s[26:27], s[22:23], 19
	s_add_u32 s23, s30, s26
	s_addc_u32 s59, s31, s27
	s_ashr_i32 s21, s20, 31
	s_lshl_b64 s[26:27], s[20:21], 19
	s_add_u32 s21, s37, s26
	s_addc_u32 s60, s38, s27
	s_mov_b32 s61, 2
	s_mov_b64 s[26:27], 0x40080
	s_cmp_lg_u32 s101, 0
	s_cbranch_scc0 .Lrob_0
	s_barrier
	s_mov_b32 s101, 0
.Lrob_0:
	s_mov_b32 s100, 1

.LBB0_265:
	s_andn2_b64 vcc, exec, s[6:7]
	s_cbranch_vccnz .LBB0_247
	s_mov_b32 s101, 1
	s_branch .LBB0_247

.LBB0_285:
	s_mov_b64 s[20:21], 0
	s_add_u32 s10, s10, s20
	s_addc_u32 s11, s11, s21
	s_add_u32 s18, s18, s20
	s_addc_u32 s19, s19, s21
	s_mov_b32 s55, 16
	s_cmp_lt_i32 s55, 1
	s_cbranch_scc1 .LBB0_291
	s_ashr_i32 s17, s16, 31
	s_lshl_b64 s[20:21], s[16:17], 19
	s_add_u32 s17, s31, s20
	s_addc_u32 s22, s37, s21
	s_and_b64 s[20:21], exec, s[4:5]
	s_cselect_b32 s21, s11, s22
	s_cselect_b32 s20, s10, s17
	s_cselect_b32 s23, s19, s1
	s_cselect_b32 s22, s18, s0
	s_lshl_b32 s17, s54, 8
	s_mov_b32 s56, 2
	s_mov_b64 s[24:25], 0x40080
	s_cmp_lg_u32 s101, 0
	s_cbranch_scc0 .Lrob_1
	s_barrier
	s_mov_b32 s101, 0

.LBB0_294:
	v_mov_b32_e32 v130, v0
	s_lshl_b32 s5, s45, 8
	v_lshrrev_b32_e32 v132, 1, v130
	s_and_b32 s5, s5, 0x3f00
	v_and_b32_e32 v132, 0x78, v132
	v_or_b32_e32 v134, s5, v132
	s_lshl_b32 s5, s45, 3
	s_lshl_b32 s4, s12, 8
	s_and_b32 s5, s5, 0xfffffe00
	v_ashrrev_i32_e32 v131, 2, v130
	s_add_i32 s5, s5, s4
	v_and_b32_e32 v131, 0xffffffc0, v131
	v_and_or_b32 v130, v130, 15, s5
	v_add_u32_e32 v130, v130, v131
	v_ashrrev_i32_e32 v131, 31, v130
	v_lshlrev_b64 v[132:133], 15, v[130:131]
	v_lshl_add_u64 v[132:133], s[8:9], 0, v[132:133]
	v_lshlrev_b32_e32 v134, 1, v134
	v_mov_b32_e32 v135, v195
	v_lshl_add_u64 v[132:133], v[132:133], 0, v[134:135]
	v_cvt_pk_bf16_f32 v126, v126, v127
	v_cvt_pk_bf16_f32 v127, v128, v129
	v_cvt_pk_bf16_f32 v128, v122, v123
	v_cvt_pk_bf16_f32 v129, v124, v125
	global_store_dwordx4 v[132:133], v[126:129], off
	v_cvt_pk_bf16_f32 v118, v118, v119
	v_cvt_pk_bf16_f32 v119, v120, v121
	v_cvt_pk_bf16_f32 v120, v114, v115
	v_or_b32_e32 v114, 16, v130
	v_ashrrev_i32_e32 v115, 31, v114
	v_lshlrev_b64 v[114:115], 15, v[114:115]
	v_lshl_add_u64 v[114:115], s[8:9], 0, v[114:115]
	v_lshl_add_u64 v[114:115], v[114:115], 0, v[134:135]
	v_cvt_pk_bf16_f32 v121, v116, v117
	global_store_dwordx4 v[132:133], v[118:121], off offset:256
	v_cvt_pk_bf16_f32 v110, v110, v111
	v_cvt_pk_bf16_f32 v111, v112, v113
	v_cvt_pk_bf16_f32 v112, v106, v107
	v_cvt_pk_bf16_f32 v113, v108, v109
	global_store_dwordx4 v[114:115], v[110:113], off
	v_cvt_pk_bf16_f32 v102, v102, v103
	v_cvt_pk_bf16_f32 v103, v104, v105
	v_cvt_pk_bf16_f32 v104, v98, v99
	v_or_b32_e32 v98, 32, v130
	v_ashrrev_i32_e32 v99, 31, v98
	v_lshlrev_b64 v[98:99], 15, v[98:99]
	v_lshl_add_u64 v[98:99], s[8:9], 0, v[98:99]
	v_lshl_add_u64 v[98:99], v[98:99], 0, v[134:135]
	v_cvt_pk_bf16_f32 v105, v100, v101
	global_store_dwordx4 v[114:115], v[102:105], off offset:256
	v_cvt_pk_bf16_f32 v94, v94, v95
	v_cvt_pk_bf16_f32 v95, v96, v97
	v_cvt_pk_bf16_f32 v96, v90, v91
	v_cvt_pk_bf16_f32 v97, v92, v93
	global_store_dwordx4 v[98:99], v[94:97], off
	v_cvt_pk_bf16_f32 v86, v86, v87
	v_cvt_pk_bf16_f32 v87, v88, v89
	v_cvt_pk_bf16_f32 v88, v82, v83
	v_or_b32_e32 v82, 48, v130
	v_ashrrev_i32_e32 v83, 31, v82
	v_lshlrev_b64 v[82:83], 15, v[82:83]
	v_lshl_add_u64 v[82:83], s[8:9], 0, v[82:83]
	v_lshl_add_u64 v[82:83], v[82:83], 0, v[134:135]
	s_mov_b64 s[4:5], 0x400000
	v_cvt_pk_bf16_f32 v89, v84, v85
	global_store_dwordx4 v[98:99], v[86:89], off offset:256
	v_cvt_pk_bf16_f32 v78, v78, v79
	v_cvt_pk_bf16_f32 v79, v80, v81
	v_cvt_pk_bf16_f32 v80, v74, v75
	v_cvt_pk_bf16_f32 v81, v76, v77
	global_store_dwordx4 v[82:83], v[78:81], off
	v_cvt_pk_bf16_f32 v70, v70, v71
	v_cvt_pk_bf16_f32 v71, v72, v73
	v_cvt_pk_bf16_f32 v72, v66, v67
	v_lshl_add_u64 v[66:67], v[132:133], 0, s[4:5]
	s_mov_b32 s4, 0x400000
	v_cvt_pk_bf16_f32 v73, v68, v69
	global_store_dwordx4 v[82:83], v[70:73], off offset:256
	v_cvt_pk_bf16_f32 v62, v62, v63
	v_cvt_pk_bf16_f32 v63, v64, v65
	v_cvt_pk_bf16_f32 v64, v58, v59
	v_add_co_u32_e32 v58, vcc, s4, v132
	s_mov_b64 s[4:5], 0x480000
	s_nop 0
	v_addc_co_u32_e32 v59, vcc, 0, v133, vcc
	v_cvt_pk_bf16_f32 v65, v60, v61
	global_store_dwordx4 v[58:59], v[62:65], off
	v_cvt_pk_bf16_f32 v54, v54, v55
	v_cvt_pk_bf16_f32 v55, v56, v57
	v_cvt_pk_bf16_f32 v56, v50, v51
	v_lshl_add_u64 v[50:51], v[132:133], 0, s[4:5]
	s_mov_b32 s4, 0x480000
	v_cvt_pk_bf16_f32 v57, v52, v53
	global_store_dwordx4 v[66:67], v[54:57], off offset:256
	v_cvt_pk_bf16_f32 v46, v46, v47
	v_cvt_pk_bf16_f32 v47, v48, v49
	v_cvt_pk_bf16_f32 v48, v42, v43
	v_add_co_u32_e32 v42, vcc, s4, v132
	s_mov_b64 s[4:5], 0x500000
	s_nop 0
	v_addc_co_u32_e32 v43, vcc, 0, v133, vcc
	v_cvt_pk_bf16_f32 v49, v44, v45
	global_store_dwordx4 v[42:43], v[46:49], off
	v_cvt_pk_bf16_f32 v38, v38, v39
	v_cvt_pk_bf16_f32 v39, v40, v41
	v_cvt_pk_bf16_f32 v40, v34, v35
	v_lshl_add_u64 v[34:35], v[132:133], 0, s[4:5]
	s_mov_b32 s4, 0x500000
	v_cvt_pk_bf16_f32 v41, v36, v37
	global_store_dwordx4 v[50:51], v[38:41], off offset:256
	v_cvt_pk_bf16_f32 v30, v30, v31
	v_cvt_pk_bf16_f32 v31, v32, v33
	v_cvt_pk_bf16_f32 v32, v26, v27
	v_add_co_u32_e32 v26, vcc, s4, v132
	v_cvt_pk_bf16_f32 v33, v28, v29
	s_mov_b64 s[4:5], 0x580000
	s_nop 0
	v_addc_co_u32_e32 v27, vcc, 0, v133, vcc
	global_store_dwordx4 v[26:27], v[30:33], off
	v_cvt_pk_bf16_f32 v22, v22, v23
	v_cvt_pk_bf16_f32 v23, v24, v25
	v_cvt_pk_bf16_f32 v24, v18, v19
	v_cvt_pk_bf16_f32 v25, v20, v21
	global_store_dwordx4 v[34:35], v[22:25], off offset:256
	v_cvt_pk_bf16_f32 v14, v14, v15
	v_cvt_pk_bf16_f32 v15, v16, v17
	v_cvt_pk_bf16_f32 v16, v10, v11
	v_add_co_u32_e32 v10, vcc, 0x580000, v132
	v_lshl_add_u64 v[18:19], v[132:133], 0, s[4:5]
	s_nop 0
	v_addc_co_u32_e32 v11, vcc, 0, v133, vcc
	s_andn2_b64 vcc, exec, s[2:3]
	s_mov_b64 s[2:3], -1
	v_cvt_pk_bf16_f32 v17, v12, v13
	global_store_dwordx4 v[10:11], v[14:17], off
	v_cvt_pk_bf16_f32 v6, v6, v7
	v_cvt_pk_bf16_f32 v7, v8, v9
	v_cvt_pk_bf16_f32 v8, v2, v3
	v_cvt_pk_bf16_f32 v9, v4, v5
	global_store_dwordx4 v[18:19], v[6:9], off offset:256
	s_cbranch_vccnz .LBB0_278
	s_andn2_b64 vcc, exec, s[6:7]
	s_cbranch_vccnz .LBB0_277
	s_mov_b32 s101, 1
	s_branch .LBB0_277

.LBB0_372:
	s_mov_b64 s[24:25], 0
	s_add_u32 s20, s20, s24
	s_addc_u32 s21, s21, s25
	s_add_u32 s8, s8, s24
	s_addc_u32 s9, s9, s25
	s_mov_b32 s54, 2
	s_cmp_lt_i32 s54, 1
	s_cbranch_scc1 .LBB0_380
	s_ashr_i32 s23, s22, 31
	s_lshl_b64 s[24:25], s[22:23], 16
	s_add_u32 s23, s30, s24
	s_addc_u32 s55, s31, s25
	s_mov_b32 s56, 2
	s_mov_b64 s[24:25], 0x8080
	s_cmp_lg_u32 s101, 0
	s_cbranch_scc0 .Lrob_2
	s_barrier
	s_mov_b32 s101, 0

.LBB0_377:
	v_mov_b32_e32 v130, v0
	v_mov_b32_e32 v131, v195
	v_and_b32_e32 v197, 15, v130
	v_ashrrev_i32_e32 v196, 8, v130
	v_lshrrev_b32_e32 v130, 1, v130
	v_lshlrev_b32_e32 v134, 7, v197
	v_and_b32_e32 v202, 0x78, v130
	v_lshl_or_b32 v134, v196, 13, v134
	v_lshlrev_b32_e32 v130, 2, v202
	v_ashrrev_i32_e32 v135, 31, v134
	v_lshl_add_u64 v[132:133], s[14:15], 0, v[130:131]
	v_lshlrev_b64 v[136:137], 2, v[134:135]
	v_lshl_add_u64 v[130:131], s[16:17], 0, v[130:131]
	v_lshl_add_u64 v[138:139], v[132:133], 0, v[136:137]
	v_lshl_add_u64 v[136:137], v[130:131], 0, v[136:137]
	global_load_dwordx4 v[178:181], v[138:139], off offset:16
	global_load_dwordx4 v[186:189], v[138:139], off
	global_load_dwordx4 v[182:185], v[136:137], off offset:16
	global_load_dwordx4 v[190:193], v[136:137], off
	v_or_b32_e32 v136, 0x800, v134
	v_ashrrev_i32_e32 v137, 31, v136
	v_lshlrev_b64 v[136:137], 2, v[136:137]
	v_lshl_add_u64 v[138:139], v[132:133], 0, v[136:137]
	v_lshl_add_u64 v[136:137], v[130:131], 0, v[136:137]
	global_load_dwordx4 v[170:173], v[138:139], off
	global_load_dwordx4 v[162:165], v[136:137], off offset:16
	global_load_dwordx4 v[174:177], v[136:137], off
	global_load_dwordx4 v[166:169], v[138:139], off offset:16
	v_or_b32_e32 v136, 0x1000, v134
	v_ashrrev_i32_e32 v137, 31, v136
	v_lshlrev_b64 v[136:137], 2, v[136:137]
	v_lshl_add_u64 v[138:139], v[132:133], 0, v[136:137]
	v_lshl_add_u64 v[136:137], v[130:131], 0, v[136:137]
	global_load_dwordx4 v[146:149], v[138:139], off offset:16
	global_load_dwordx4 v[154:157], v[138:139], off
	global_load_dwordx4 v[150:153], v[136:137], off offset:16
	global_load_dwordx4 v[158:161], v[136:137], off
	v_or_b32_e32 v134, 0x1800, v134
	v_ashrrev_i32_e32 v135, 31, v134
	v_lshlrev_b64 v[134:135], 2, v[134:135]
	v_lshl_add_u64 v[136:137], v[132:133], 0, v[134:135]
	v_lshl_add_u64 v[142:143], v[130:131], 0, v[134:135]
	global_load_dwordx4 v[130:133], v[136:137], off offset:16
	global_load_dwordx4 v[138:141], v[136:137], off
	s_nop 0
	global_load_dwordx4 v[134:137], v[142:143], off offset:16
	s_nop 0
	global_load_dwordx4 v[142:145], v[142:143], off
	s_lshl_b32 s23, s53, 8
	v_lshl_add_u32 v196, v196, 6, s23
	v_or_b32_e32 v222, v196, v197
	v_ashrrev_i32_e32 v223, 31, v222
	s_mov_b64 s[24:25], -1
	s_andn2_b64 vcc, exec, s[2:3]
	s_waitcnt vmcnt(0)
	v_pk_mul_f32 v[196:197], v[120:121], v[192:193]
	v_pk_mul_f32 v[198:199], v[118:119], v[190:191]
	v_pk_fma_f32 v[196:197], v[128:129], v[188:189], v[196:197]
	v_pk_fma_f32 v[198:199], v[126:127], v[186:187], v[198:199]
	v_pk_mul_f32 v[128:129], v[128:129], v[192:193]
	v_pk_mul_f32 v[126:127], v[126:127], v[190:191]
	v_pk_fma_f32 v[120:121], v[120:121], v[188:189], v[128:129] neg_lo:[0,0,1] neg_hi:[0,0,1]
	v_pk_fma_f32 v[126:127], v[118:119], v[186:187], v[126:127] neg_lo:[0,0,1] neg_hi:[0,0,1]
	v_pk_mul_f32 v[118:119], v[116:117], v[184:185]
	v_pk_mul_f32 v[128:129], v[114:115], v[182:183]
	v_pk_fma_f32 v[200:201], v[124:125], v[180:181], v[118:119]
	v_pk_fma_f32 v[118:119], v[122:123], v[178:179], v[128:129]
	v_pk_mul_f32 v[122:123], v[122:123], v[182:183]
	v_pk_mul_f32 v[124:125], v[124:125], v[184:185]
	v_pk_fma_f32 v[122:123], v[114:115], v[178:179], v[122:123] neg_lo:[0,0,1] neg_hi:[0,0,1]
	v_lshlrev_b64 v[114:115], 9, v[222:223]
	v_pk_fma_f32 v[124:125], v[116:117], v[180:181], v[124:125] neg_lo:[0,0,1] neg_hi:[0,0,1]
	v_lshl_add_u64 v[116:117], s[12:13], 0, v[114:115]
	v_lshlrev_b32_e32 v114, 1, v202
	v_mov_b32_e32 v115, v195
	v_lshl_add_u64 v[128:129], v[116:117], 0, v[114:115]
	v_cvt_pk_bf16_f32 v116, v198, v199
	v_cvt_pk_bf16_f32 v117, v196, v197
	v_cvt_pk_bf16_f32 v118, v118, v119
	v_cvt_pk_bf16_f32 v119, v200, v201
	global_store_dwordx4 v[128:129], v[116:119], off
	s_nop 1
	v_cvt_pk_bf16_f32 v116, v126, v127
	v_cvt_pk_bf16_f32 v117, v120, v121
	v_cvt_pk_bf16_f32 v118, v122, v123
	v_cvt_pk_bf16_f32 v119, v124, v125
	global_store_dwordx4 v[128:129], v[116:119], off offset:256
	s_nop 1
	v_pk_mul_f32 v[116:117], v[108:109], v[192:193]
	v_pk_mul_f32 v[118:119], v[106:107], v[190:191]
	v_pk_fma_f32 v[116:117], v[112:113], v[188:189], v[116:117]
	v_pk_mul_f32 v[112:113], v[112:113], v[192:193]
	v_pk_fma_f32 v[118:119], v[110:111], v[186:187], v[118:119]
	v_pk_fma_f32 v[108:109], v[108:109], v[188:189], v[112:113] neg_lo:[0,0,1] neg_hi:[0,0,1]
	v_pk_mul_f32 v[112:113], v[98:99], v[182:183]
	v_pk_mul_f32 v[110:111], v[110:111], v[190:191]
	v_pk_fma_f32 v[112:113], v[102:103], v[178:179], v[112:113]
	v_pk_mul_f32 v[102:103], v[102:103], v[182:183]
	v_pk_fma_f32 v[106:107], v[106:107], v[186:187], v[110:111] neg_lo:[0,0,1] neg_hi:[0,0,1]
	v_pk_fma_f32 v[102:103], v[98:99], v[178:179], v[102:103] neg_lo:[0,0,1] neg_hi:[0,0,1]
	v_add_u32_e32 v98, 0x80, v222
	v_ashrrev_i32_e32 v99, 31, v98
	v_pk_mul_f32 v[110:111], v[100:101], v[184:185]
	v_lshlrev_b64 v[98:99], 9, v[98:99]
	v_pk_fma_f32 v[110:111], v[104:105], v[180:181], v[110:111]
	v_pk_mul_f32 v[104:105], v[104:105], v[184:185]
	v_lshl_add_u64 v[98:99], s[12:13], 0, v[98:99]
	v_pk_fma_f32 v[104:105], v[100:101], v[180:181], v[104:105] neg_lo:[0,0,1] neg_hi:[0,0,1]
	v_lshl_add_u64 v[120:121], v[98:99], 0, v[114:115]
	v_cvt_pk_bf16_f32 v98, v118, v119
	v_cvt_pk_bf16_f32 v99, v116, v117
	v_cvt_pk_bf16_f32 v100, v112, v113
	v_cvt_pk_bf16_f32 v101, v110, v111
	global_store_dwordx4 v[120:121], v[98:101], off
	s_nop 1
	v_cvt_pk_bf16_f32 v98, v106, v107
	v_cvt_pk_bf16_f32 v99, v108, v109
	v_cvt_pk_bf16_f32 v100, v102, v103
	v_cvt_pk_bf16_f32 v101, v104, v105
	global_store_dwordx4 v[120:121], v[98:101], off offset:256
	v_pk_mul_f32 v[102:103], v[90:91], v[174:175]
	s_nop 0
	v_pk_mul_f32 v[100:101], v[92:93], v[176:177]
	v_or_b32_e32 v98, 16, v222
	v_pk_fma_f32 v[100:101], v[96:97], v[172:173], v[100:101]
	v_pk_mul_f32 v[96:97], v[96:97], v[176:177]
	v_ashrrev_i32_e32 v99, 31, v98
	v_pk_fma_f32 v[92:93], v[92:93], v[172:173], v[96:97] neg_lo:[0,0,1] neg_hi:[0,0,1]
	v_pk_mul_f32 v[96:97], v[82:83], v[162:163]
	v_pk_fma_f32 v[102:103], v[94:95], v[170:171], v[102:103]
	v_pk_fma_f32 v[96:97], v[86:87], v[166:167], v[96:97]
	v_pk_mul_f32 v[86:87], v[86:87], v[162:163]
	v_pk_mul_f32 v[94:95], v[94:95], v[174:175]
	v_pk_fma_f32 v[86:87], v[82:83], v[166:167], v[86:87] neg_lo:[0,0,1] neg_hi:[0,0,1]
	v_lshlrev_b64 v[82:83], 9, v[98:99]
	v_pk_fma_f32 v[90:91], v[90:91], v[170:171], v[94:95] neg_lo:[0,0,1] neg_hi:[0,0,1]
	v_pk_mul_f32 v[94:95], v[84:85], v[164:165]
	v_lshl_add_u64 v[82:83], s[12:13], 0, v[82:83]
	v_pk_fma_f32 v[94:95], v[88:89], v[168:169], v[94:95]
	v_pk_mul_f32 v[88:89], v[88:89], v[164:165]
	v_lshl_add_u64 v[98:99], v[82:83], 0, v[114:115]
	v_cvt_pk_bf16_f32 v82, v102, v103
	v_cvt_pk_bf16_f32 v83, v100, v101
	v_pk_fma_f32 v[88:89], v[84:85], v[168:169], v[88:89] neg_lo:[0,0,1] neg_hi:[0,0,1]
	v_cvt_pk_bf16_f32 v84, v96, v97
	v_cvt_pk_bf16_f32 v85, v94, v95
	global_store_dwordx4 v[98:99], v[82:85], off
	s_nop 1
	v_cvt_pk_bf16_f32 v82, v90, v91
	v_cvt_pk_bf16_f32 v83, v92, v93
	v_cvt_pk_bf16_f32 v84, v86, v87
	v_cvt_pk_bf16_f32 v85, v88, v89
	global_store_dwordx4 v[98:99], v[82:85], off offset:256
	s_nop 1
	v_pk_mul_f32 v[82:83], v[76:77], v[176:177]
	v_pk_mul_f32 v[84:85], v[74:75], v[174:175]
	v_pk_fma_f32 v[82:83], v[80:81], v[172:173], v[82:83]
	v_pk_mul_f32 v[80:81], v[80:81], v[176:177]
	v_pk_fma_f32 v[84:85], v[78:79], v[170:171], v[84:85]
	v_pk_fma_f32 v[76:77], v[76:77], v[172:173], v[80:81] neg_lo:[0,0,1] neg_hi:[0,0,1]
	v_pk_mul_f32 v[80:81], v[66:67], v[162:163]
	v_pk_mul_f32 v[78:79], v[78:79], v[174:175]
	v_pk_fma_f32 v[80:81], v[70:71], v[166:167], v[80:81]
	v_pk_mul_f32 v[70:71], v[70:71], v[162:163]
	v_pk_fma_f32 v[74:75], v[74:75], v[170:171], v[78:79] neg_lo:[0,0,1] neg_hi:[0,0,1]
	v_pk_fma_f32 v[70:71], v[66:67], v[166:167], v[70:71] neg_lo:[0,0,1] neg_hi:[0,0,1]
	v_add_u32_e32 v66, 0x90, v222
	v_ashrrev_i32_e32 v67, 31, v66
	v_pk_mul_f32 v[78:79], v[68:69], v[164:165]
	v_lshlrev_b64 v[66:67], 9, v[66:67]
	v_pk_fma_f32 v[78:79], v[72:73], v[168:169], v[78:79]
	v_pk_mul_f32 v[72:73], v[72:73], v[164:165]
	v_lshl_add_u64 v[66:67], s[12:13], 0, v[66:67]
	v_pk_fma_f32 v[72:73], v[68:69], v[168:169], v[72:73] neg_lo:[0,0,1] neg_hi:[0,0,1]
	v_lshl_add_u64 v[86:87], v[66:67], 0, v[114:115]
	v_cvt_pk_bf16_f32 v66, v84, v85
	v_cvt_pk_bf16_f32 v67, v82, v83
	v_cvt_pk_bf16_f32 v68, v80, v81
	v_cvt_pk_bf16_f32 v69, v78, v79
	global_store_dwordx4 v[86:87], v[66:69], off
	s_nop 1
	v_cvt_pk_bf16_f32 v66, v74, v75
	v_cvt_pk_bf16_f32 v67, v76, v77
	v_cvt_pk_bf16_f32 v68, v70, v71
	v_cvt_pk_bf16_f32 v69, v72, v73
	global_store_dwordx4 v[86:87], v[66:69], off offset:256
	v_pk_mul_f32 v[70:71], v[58:59], v[158:159]
	s_nop 0
	v_pk_mul_f32 v[68:69], v[60:61], v[160:161]
	v_or_b32_e32 v66, 32, v222
	v_pk_fma_f32 v[68:69], v[64:65], v[156:157], v[68:69]
	v_pk_mul_f32 v[64:65], v[64:65], v[160:161]
	v_ashrrev_i32_e32 v67, 31, v66
	v_pk_fma_f32 v[60:61], v[60:61], v[156:157], v[64:65] neg_lo:[0,0,1] neg_hi:[0,0,1]
	v_pk_mul_f32 v[64:65], v[50:51], v[150:151]
	v_pk_fma_f32 v[70:71], v[62:63], v[154:155], v[70:71]
	v_pk_fma_f32 v[64:65], v[54:55], v[146:147], v[64:65]
	v_pk_mul_f32 v[54:55], v[54:55], v[150:151]
	v_pk_mul_f32 v[62:63], v[62:63], v[158:159]
	v_pk_fma_f32 v[54:55], v[50:51], v[146:147], v[54:55] neg_lo:[0,0,1] neg_hi:[0,0,1]
	v_lshlrev_b64 v[50:51], 9, v[66:67]
	v_pk_fma_f32 v[58:59], v[58:59], v[154:155], v[62:63] neg_lo:[0,0,1] neg_hi:[0,0,1]
	v_pk_mul_f32 v[62:63], v[52:53], v[152:153]
	v_lshl_add_u64 v[50:51], s[12:13], 0, v[50:51]
	v_pk_fma_f32 v[62:63], v[56:57], v[148:149], v[62:63]
	v_pk_mul_f32 v[56:57], v[56:57], v[152:153]
	v_lshl_add_u64 v[66:67], v[50:51], 0, v[114:115]
	v_cvt_pk_bf16_f32 v50, v70, v71
	v_cvt_pk_bf16_f32 v51, v68, v69
	v_pk_fma_f32 v[56:57], v[52:53], v[148:149], v[56:57] neg_lo:[0,0,1] neg_hi:[0,0,1]
	v_cvt_pk_bf16_f32 v52, v64, v65
	v_cvt_pk_bf16_f32 v53, v62, v63
	global_store_dwordx4 v[66:67], v[50:53], off
	s_nop 1
	v_cvt_pk_bf16_f32 v50, v58, v59
	v_cvt_pk_bf16_f32 v51, v60, v61
	v_cvt_pk_bf16_f32 v52, v54, v55
	v_cvt_pk_bf16_f32 v53, v56, v57
	global_store_dwordx4 v[66:67], v[50:53], off offset:256
	s_nop 1
	v_pk_mul_f32 v[50:51], v[44:45], v[160:161]
	v_pk_mul_f32 v[52:53], v[42:43], v[158:159]
	v_pk_fma_f32 v[50:51], v[48:49], v[156:157], v[50:51]
	v_pk_mul_f32 v[48:49], v[48:49], v[160:161]
	v_pk_fma_f32 v[52:53], v[46:47], v[154:155], v[52:53]
	v_pk_fma_f32 v[44:45], v[44:45], v[156:157], v[48:49] neg_lo:[0,0,1] neg_hi:[0,0,1]
	v_pk_mul_f32 v[48:49], v[34:35], v[150:151]
	v_pk_mul_f32 v[46:47], v[46:47], v[158:159]
	v_pk_fma_f32 v[48:49], v[38:39], v[146:147], v[48:49]
	v_pk_mul_f32 v[38:39], v[38:39], v[150:151]
	v_pk_fma_f32 v[42:43], v[42:43], v[154:155], v[46:47] neg_lo:[0,0,1] neg_hi:[0,0,1]
	v_pk_fma_f32 v[38:39], v[34:35], v[146:147], v[38:39] neg_lo:[0,0,1] neg_hi:[0,0,1]
	v_add_u32_e32 v34, 0xa0, v222
	v_ashrrev_i32_e32 v35, 31, v34
	v_pk_mul_f32 v[46:47], v[36:37], v[152:153]
	v_lshlrev_b64 v[34:35], 9, v[34:35]
	v_pk_fma_f32 v[46:47], v[40:41], v[148:149], v[46:47]
	v_pk_mul_f32 v[40:41], v[40:41], v[152:153]
	v_lshl_add_u64 v[34:35], s[12:13], 0, v[34:35]
	v_pk_fma_f32 v[40:41], v[36:37], v[148:149], v[40:41] neg_lo:[0,0,1] neg_hi:[0,0,1]
	v_lshl_add_u64 v[54:55], v[34:35], 0, v[114:115]
	v_cvt_pk_bf16_f32 v34, v52, v53
	v_cvt_pk_bf16_f32 v35, v50, v51
	v_cvt_pk_bf16_f32 v36, v48, v49
	v_cvt_pk_bf16_f32 v37, v46, v47
	global_store_dwordx4 v[54:55], v[34:37], off
	s_nop 1
	v_cvt_pk_bf16_f32 v34, v42, v43
	v_cvt_pk_bf16_f32 v35, v44, v45
	v_cvt_pk_bf16_f32 v36, v38, v39
	v_cvt_pk_bf16_f32 v37, v40, v41
	global_store_dwordx4 v[54:55], v[34:37], off offset:256
	v_pk_mul_f32 v[38:39], v[26:27], v[142:143]
	s_nop 0
	v_pk_mul_f32 v[36:37], v[28:29], v[144:145]
	v_or_b32_e32 v34, 48, v222
	v_pk_fma_f32 v[36:37], v[32:33], v[140:141], v[36:37]
	v_pk_mul_f32 v[32:33], v[32:33], v[144:145]
	v_ashrrev_i32_e32 v35, 31, v34
	v_pk_fma_f32 v[28:29], v[28:29], v[140:141], v[32:33] neg_lo:[0,0,1] neg_hi:[0,0,1]
	v_pk_mul_f32 v[32:33], v[18:19], v[134:135]
	v_pk_fma_f32 v[38:39], v[30:31], v[138:139], v[38:39]
	v_pk_fma_f32 v[32:33], v[22:23], v[130:131], v[32:33]
	v_pk_mul_f32 v[22:23], v[22:23], v[134:135]
	v_pk_mul_f32 v[30:31], v[30:31], v[142:143]
	v_pk_fma_f32 v[22:23], v[18:19], v[130:131], v[22:23] neg_lo:[0,0,1] neg_hi:[0,0,1]
	v_lshlrev_b64 v[18:19], 9, v[34:35]
	v_pk_fma_f32 v[26:27], v[26:27], v[138:139], v[30:31] neg_lo:[0,0,1] neg_hi:[0,0,1]
	v_pk_mul_f32 v[30:31], v[20:21], v[136:137]
	v_lshl_add_u64 v[18:19], s[12:13], 0, v[18:19]
	v_pk_fma_f32 v[30:31], v[24:25], v[132:133], v[30:31]
	v_pk_mul_f32 v[24:25], v[24:25], v[136:137]
	v_lshl_add_u64 v[34:35], v[18:19], 0, v[114:115]
	v_cvt_pk_bf16_f32 v18, v38, v39
	v_cvt_pk_bf16_f32 v19, v36, v37
	v_pk_fma_f32 v[24:25], v[20:21], v[132:133], v[24:25] neg_lo:[0,0,1] neg_hi:[0,0,1]
	v_cvt_pk_bf16_f32 v20, v32, v33
	v_cvt_pk_bf16_f32 v21, v30, v31
	global_store_dwordx4 v[34:35], v[18:21], off
	s_nop 1
	v_cvt_pk_bf16_f32 v18, v26, v27
	v_cvt_pk_bf16_f32 v19, v28, v29
	v_cvt_pk_bf16_f32 v20, v22, v23
	v_cvt_pk_bf16_f32 v21, v24, v25
	global_store_dwordx4 v[34:35], v[18:21], off offset:256
	s_nop 1
	v_pk_mul_f32 v[18:19], v[12:13], v[144:145]
	v_pk_mul_f32 v[20:21], v[10:11], v[142:143]
	v_pk_fma_f32 v[18:19], v[16:17], v[140:141], v[18:19]
	v_pk_mul_f32 v[16:17], v[16:17], v[144:145]
	v_pk_fma_f32 v[20:21], v[14:15], v[138:139], v[20:21]
	v_pk_fma_f32 v[12:13], v[12:13], v[140:141], v[16:17] neg_lo:[0,0,1] neg_hi:[0,0,1]
	v_pk_mul_f32 v[16:17], v[2:3], v[134:135]
	v_pk_mul_f32 v[14:15], v[14:15], v[142:143]
	v_pk_fma_f32 v[16:17], v[6:7], v[130:131], v[16:17]
	v_pk_mul_f32 v[6:7], v[6:7], v[134:135]
	v_pk_fma_f32 v[10:11], v[10:11], v[138:139], v[14:15] neg_lo:[0,0,1] neg_hi:[0,0,1]
	v_pk_fma_f32 v[6:7], v[2:3], v[130:131], v[6:7] neg_lo:[0,0,1] neg_hi:[0,0,1]
	v_add_u32_e32 v2, 0xb0, v222
	v_ashrrev_i32_e32 v3, 31, v2
	v_pk_mul_f32 v[14:15], v[4:5], v[136:137]
	v_lshlrev_b64 v[2:3], 9, v[2:3]
	v_pk_fma_f32 v[14:15], v[8:9], v[132:133], v[14:15]
	v_pk_mul_f32 v[8:9], v[8:9], v[136:137]
	v_lshl_add_u64 v[2:3], s[12:13], 0, v[2:3]
	v_pk_fma_f32 v[8:9], v[4:5], v[132:133], v[8:9] neg_lo:[0,0,1] neg_hi:[0,0,1]
	v_lshl_add_u64 v[22:23], v[2:3], 0, v[114:115]
	v_cvt_pk_bf16_f32 v2, v20, v21
	v_cvt_pk_bf16_f32 v3, v18, v19
	v_cvt_pk_bf16_f32 v4, v16, v17
	v_cvt_pk_bf16_f32 v5, v14, v15
	global_store_dwordx4 v[22:23], v[2:5], off
	s_nop 1
	v_cvt_pk_bf16_f32 v2, v10, v11
	v_cvt_pk_bf16_f32 v3, v12, v13
	v_cvt_pk_bf16_f32 v4, v6, v7
	v_cvt_pk_bf16_f32 v5, v8, v9
	global_store_dwordx4 v[22:23], v[2:5], off offset:256
	s_cbranch_vccnz .LBB0_365
	s_andn2_b64 vcc, exec, s[10:11]
	s_cbranch_vccnz .LBB0_364
	s_mov_b32 s101, 1
	s_branch .LBB0_364

.LBB0_490:
	s_mov_b64 s[18:19], 0
	s_add_u32 s16, s16, s18
	s_addc_u32 s17, s17, s19
	s_add_u32 s14, s14, s18
	s_addc_u32 s15, s15, s19
	s_mov_b32 s52, 4
	s_cmp_lt_i32 s52, 1
	s_cbranch_scc1 .LBB0_496
	s_and_b64 s[18:19], exec, s[4:5]
	s_cselect_b32 s19, s17, s1
	s_cselect_b32 s18, s16, s0
	s_cselect_b32 s21, s15, s7
	s_cselect_b32 s20, s14, s6
	s_lshl_b32 s22, s51, 1
	s_and_b32 s53, s22, 0x7e
	s_and_b32 s54, s22, 0xff80
	s_mov_b32 s55, 2
	s_mov_b64 s[22:23], 0x10080
	s_cmp_lg_u32 s101, 0
	s_cbranch_scc0 .Lrob_3
	s_barrier
	s_mov_b32 s101, 0

.LBB0_499:
	v_mov_b32_e32 v130, v0
	s_lshl_b32 s4, s42, 1
	v_lshrrev_b32_e32 v131, 1, v130
	s_and_b32 s5, s4, 0x7e
	s_and_b32 s4, s4, 0x180
	v_and_b32_e32 v131, 0x78, v131
	v_or_b32_e32 v131, s4, v131
	s_lshl_b32 s4, s42, 6
	s_and_b32 s4, s4, 0xffffc000
	v_lshlrev_b32_e32 v132, 5, v130
	v_lshlrev_b32_e32 v130, 7, v130
	s_or_b32 s4, s4, s5
	v_and_b32_e32 v130, 0x780, v130
	s_movk_i32 s5, 0xe000
	v_and_or_b32 v130, v132, s5, v130
	v_add_u32_e32 v132, s4, v130
	v_cvt_pk_bf16_f32 v126, v126, v127
	v_cvt_pk_bf16_f32 v127, v128, v129
	v_cvt_pk_bf16_f32 v128, v122, v123
	v_mov_b64_e32 v[122:123], s[10:11]
	v_cvt_pk_bf16_f32 v129, v124, v125
	v_mad_i64_i32 v[124:125], s[4:5], v132, s34, v[122:123]
	v_lshlrev_b32_e32 v130, 1, v131
	v_mov_b32_e32 v131, v195
	v_lshl_add_u64 v[124:125], v[124:125], 0, v[130:131]
	global_store_dwordx4 v[124:125], v[126:129], off offset:1024
	v_cvt_pk_bf16_f32 v118, v118, v119
	v_cvt_pk_bf16_f32 v119, v120, v121
	v_cvt_pk_bf16_f32 v120, v114, v115
	v_cvt_pk_bf16_f32 v121, v116, v117
	v_or_b32_e32 v116, 0x800, v132
	s_nop 0
	v_or_b32_e32 v126, 1, v132
	v_mad_i64_i32 v[114:115], s[4:5], v126, s34, v[122:123]
	v_lshl_add_u64 v[114:115], v[114:115], 0, v[130:131]
	global_store_dwordx4 v[114:115], v[118:121], off offset:1024
	v_cvt_pk_bf16_f32 v110, v110, v111
	v_cvt_pk_bf16_f32 v111, v112, v113
	v_cvt_pk_bf16_f32 v112, v106, v107
	v_mad_i64_i32 v[106:107], s[4:5], v116, s34, v[122:123]
	v_cvt_pk_bf16_f32 v113, v108, v109
	v_lshl_add_u64 v[106:107], v[106:107], 0, v[130:131]
	v_or_b32_e32 v108, 0x801, v132
	global_store_dwordx4 v[106:107], v[110:113], off offset:1024
	v_cvt_pk_bf16_f32 v102, v102, v103
	v_cvt_pk_bf16_f32 v103, v104, v105
	v_cvt_pk_bf16_f32 v104, v98, v99
	v_mad_i64_i32 v[98:99], s[4:5], v108, s34, v[122:123]
	v_cvt_pk_bf16_f32 v105, v100, v101
	v_lshl_add_u64 v[98:99], v[98:99], 0, v[130:131]
	v_or_b32_e32 v100, 0x1000, v132
	global_store_dwordx4 v[98:99], v[102:105], off offset:1024
	v_cvt_pk_bf16_f32 v94, v94, v95
	v_cvt_pk_bf16_f32 v95, v96, v97
	v_cvt_pk_bf16_f32 v96, v90, v91
	v_mad_i64_i32 v[90:91], s[4:5], v100, s34, v[122:123]
	v_cvt_pk_bf16_f32 v97, v92, v93
	v_lshl_add_u64 v[90:91], v[90:91], 0, v[130:131]
	v_or_b32_e32 v92, 0x1001, v132
	global_store_dwordx4 v[90:91], v[94:97], off offset:1024
	v_cvt_pk_bf16_f32 v86, v86, v87
	v_cvt_pk_bf16_f32 v87, v88, v89
	v_cvt_pk_bf16_f32 v88, v82, v83
	v_mad_i64_i32 v[82:83], s[4:5], v92, s34, v[122:123]
	v_cvt_pk_bf16_f32 v89, v84, v85
	v_lshl_add_u64 v[82:83], v[82:83], 0, v[130:131]
	v_or_b32_e32 v84, 0x1800, v132
	global_store_dwordx4 v[82:83], v[86:89], off offset:1024
	v_cvt_pk_bf16_f32 v78, v78, v79
	v_cvt_pk_bf16_f32 v79, v80, v81
	v_cvt_pk_bf16_f32 v80, v74, v75
	v_mad_i64_i32 v[74:75], s[4:5], v84, s34, v[122:123]
	v_cvt_pk_bf16_f32 v81, v76, v77
	v_lshl_add_u64 v[74:75], v[74:75], 0, v[130:131]
	v_or_b32_e32 v76, 0x1801, v132
	global_store_dwordx4 v[74:75], v[78:81], off offset:1024
	v_cvt_pk_bf16_f32 v70, v70, v71
	v_cvt_pk_bf16_f32 v71, v72, v73
	v_cvt_pk_bf16_f32 v72, v66, v67
	v_mad_i64_i32 v[66:67], s[4:5], v76, s34, v[122:123]
	v_lshl_add_u64 v[66:67], v[66:67], 0, v[130:131]
	s_andn2_b64 vcc, exec, s[2:3]
	s_mov_b64 s[2:3], -1
	v_cvt_pk_bf16_f32 v73, v68, v69
	global_store_dwordx4 v[66:67], v[70:73], off offset:1024
	v_cvt_pk_bf16_f32 v62, v62, v63
	v_cvt_pk_bf16_f32 v63, v64, v65
	v_cvt_pk_bf16_f32 v64, v58, v59
	v_cvt_pk_bf16_f32 v65, v60, v61
	global_store_dwordx4 v[124:125], v[62:65], off offset:2048
	v_cvt_pk_bf16_f32 v54, v54, v55
	v_cvt_pk_bf16_f32 v55, v56, v57
	v_cvt_pk_bf16_f32 v56, v50, v51
	v_cvt_pk_bf16_f32 v57, v52, v53
	global_store_dwordx4 v[114:115], v[54:57], off offset:2048
	v_cvt_pk_bf16_f32 v46, v46, v47
	v_cvt_pk_bf16_f32 v47, v48, v49
	v_cvt_pk_bf16_f32 v48, v42, v43
	v_cvt_pk_bf16_f32 v49, v44, v45
	global_store_dwordx4 v[106:107], v[46:49], off offset:2048
	v_cvt_pk_bf16_f32 v38, v38, v39
	v_cvt_pk_bf16_f32 v39, v40, v41
	v_cvt_pk_bf16_f32 v40, v34, v35
	v_cvt_pk_bf16_f32 v41, v36, v37
	global_store_dwordx4 v[98:99], v[38:41], off offset:2048
	v_cvt_pk_bf16_f32 v30, v30, v31
	v_cvt_pk_bf16_f32 v31, v32, v33
	v_cvt_pk_bf16_f32 v32, v26, v27
	v_cvt_pk_bf16_f32 v33, v28, v29
	global_store_dwordx4 v[90:91], v[30:33], off offset:2048
	v_cvt_pk_bf16_f32 v22, v22, v23
	v_cvt_pk_bf16_f32 v23, v24, v25
	v_cvt_pk_bf16_f32 v24, v18, v19
	v_cvt_pk_bf16_f32 v25, v20, v21
	global_store_dwordx4 v[82:83], v[22:25], off offset:2048
	v_cvt_pk_bf16_f32 v14, v14, v15
	v_cvt_pk_bf16_f32 v15, v16, v17
	v_cvt_pk_bf16_f32 v16, v10, v11
	v_cvt_pk_bf16_f32 v17, v12, v13
	global_store_dwordx4 v[74:75], v[14:17], off offset:2048
	v_cvt_pk_bf16_f32 v6, v6, v7
	v_cvt_pk_bf16_f32 v7, v8, v9
	v_cvt_pk_bf16_f32 v8, v2, v3
	v_cvt_pk_bf16_f32 v9, v4, v5
	global_store_dwordx4 v[66:67], v[6:9], off offset:2048
	s_cbranch_vccnz .LBB0_483
	s_andn2_b64 vcc, exec, s[8:9]
	s_cbranch_vccnz .LBB0_482
	s_mov_b32 s101, 1
	s_branch .LBB0_482

.LBB0_577:
	s_mov_b32 s58, 24
	s_cmp_lt_i32 s58, 1
	s_cbranch_scc1 .LBB0_588
	s_lshl_b32 s20, s57, 8
	s_ashr_i32 s21, s20, 31
	s_add_i32 s59, s58, -2
	s_lshl_b32 s60, s56, 8
	s_lshl_b64 s[20:21], s[20:21], 1
	s_add_u32 s20, s44, s20
	s_addc_u32 s21, s45, s21
	s_mov_b32 s61, 0
	s_mov_b64 s[22:23], 0x60080
	s_cmp_lg_u32 s101, 0
	s_cbranch_scc0 .Lrob_4
	s_barrier
	s_mov_b32 s101, 0

.LBB0_585:
	v_mov_b32_e32 v132, v0
	s_lshl_b32 s4, s57, 8
	v_ashrrev_i32_e32 v130, 2, v132
	v_and_b32_e32 v130, 0xffffffc0, v130
	v_lshl_add_u32 v130, s56, 8, v130
	v_and_or_b32 v130, v132, 15, v130
	v_ashrrev_i32_e32 v131, 31, v130
	v_lshlrev_b64 v[130:131], 10, v[130:131]
	s_ashr_i32 s5, s4, 31
	v_lshrrev_b32_e32 v132, 1, v132
	v_lshl_add_u64 v[130:131], v[130:131], 0, s[4:5]
	v_and_b32_e32 v133, 0x60, v132
	v_and_b32_e32 v132, 24, v132
	v_or3_b32 v130, v130, v133, v132
	v_lshlrev_b64 v[218:219], 1, v[130:131]
	v_lshl_add_u64 v[130:131], s[10:11], 0, v[218:219]
	global_load_dwordx4 v[196:199], v[130:131], off
	global_load_dwordx4 v[186:189], v[130:131], off offset:256
	s_mov_b32 s4, 0x8000
	v_add_co_u32_e32 v132, vcc, s4, v130
	s_mov_b32 s5, 0x18000
	s_nop 0
	v_addc_co_u32_e32 v133, vcc, 0, v131, vcc
	global_load_dwordx4 v[182:185], v[132:133], off
	global_load_dwordx4 v[178:181], v[132:133], off offset:256
	v_add_co_u32_e32 v132, vcc, s73, v130
	s_mov_b32 s16, 0x40000
	s_nop 0
	v_addc_co_u32_e32 v133, vcc, 0, v131, vcc
	global_load_dwordx4 v[174:177], v[132:133], off
	global_load_dwordx4 v[170:173], v[132:133], off offset:256
	v_add_co_u32_e32 v132, vcc, s5, v130
	s_mov_b32 s18, 0x48000
	s_nop 0
	v_addc_co_u32_e32 v133, vcc, 0, v131, vcc
	global_load_dwordx4 v[166:169], v[132:133], off
	global_load_dwordx4 v[162:165], v[132:133], off offset:256
	v_add_co_u32_e32 v132, vcc, s16, v130
	s_mov_b32 s17, 0x50000
	s_nop 0
	v_addc_co_u32_e32 v133, vcc, 0, v131, vcc
	global_load_dwordx4 v[158:161], v[132:133], off
	global_load_dwordx4 v[154:157], v[132:133], off offset:256
	v_add_co_u32_e32 v132, vcc, s18, v130
	s_mov_b32 s88, 0x40000
	s_nop 0
	v_addc_co_u32_e32 v133, vcc, 0, v131, vcc
	global_load_dwordx4 v[150:153], v[132:133], off
	global_load_dwordx4 v[146:149], v[132:133], off offset:256
	v_add_co_u32_e32 v132, vcc, s17, v130
	s_mov_b32 s94, 0x48000
	s_nop 0
	v_addc_co_u32_e32 v133, vcc, 0, v131, vcc
	global_load_dwordx4 v[142:145], v[132:133], off
	global_load_dwordx4 v[138:141], v[132:133], off offset:256
	v_add_co_u32_e32 v130, vcc, s95, v130
	s_mov_b32 s89, 0x50000
	s_nop 0
	v_addc_co_u32_e32 v131, vcc, 0, v131, vcc
	global_load_dwordx4 v[134:137], v[130:131], off
	s_nop 0
	global_load_dwordx4 v[130:133], v[130:131], off offset:256
	s_waitcnt vmcnt(0)
	v_lshlrev_b32_e32 v200, 16, v196
	v_and_b32_e32 v201, 0xffff0000, v196
	v_lshlrev_b32_e32 v202, 16, v198
	v_and_b32_e32 v203, 0xffff0000, v198
	v_lshlrev_b32_e32 v196, 16, v197
	v_and_b32_e32 v197, 0xffff0000, v197
	v_lshlrev_b32_e32 v198, 16, v199
	v_and_b32_e32 v199, 0xffff0000, v199
	v_pk_mul_f32 v[122:123], v[122:123], v[200:201]
	v_pk_mul_f32 v[126:127], v[126:127], v[202:203]
	v_pk_mul_f32 v[196:197], v[124:125], v[196:197]
	v_pk_mul_f32 v[128:129], v[128:129], v[198:199]
	v_cvt_pk_bf16_f32 v124, v122, v123
	v_cvt_pk_bf16_f32 v125, v196, v197
	v_cvt_pk_bf16_f32 v126, v126, v127
	v_lshl_add_u64 v[122:123], s[12:13], 0, v[218:219]
	v_cvt_pk_bf16_f32 v127, v128, v129
	global_store_dwordx4 v[122:123], v[124:127], off
	v_lshlrev_b32_e32 v128, 16, v188
	v_and_b32_e32 v129, 0xffff0000, v188
	v_lshlrev_b32_e32 v124, 16, v186
	v_and_b32_e32 v125, 0xffff0000, v186
	v_lshlrev_b32_e32 v126, 16, v187
	v_and_b32_e32 v127, 0xffff0000, v187
	v_lshlrev_b32_e32 v186, 16, v189
	v_and_b32_e32 v187, 0xffff0000, v189
	v_pk_mul_f32 v[120:121], v[120:121], v[126:127]
	v_pk_mul_f32 v[118:119], v[118:119], v[124:125]
	v_pk_mul_f32 v[124:125], v[116:117], v[186:187]
	v_pk_mul_f32 v[116:117], v[114:115], v[128:129]
	v_cvt_pk_bf16_f32 v114, v118, v119
	v_cvt_pk_bf16_f32 v115, v120, v121
	v_lshlrev_b32_e32 v118, 16, v184
	v_cvt_pk_bf16_f32 v116, v116, v117
	v_cvt_pk_bf16_f32 v117, v124, v125
	global_store_dwordx4 v[122:123], v[114:117], off offset:256
	v_and_b32_e32 v119, 0xffff0000, v184
	v_lshlrev_b32_e32 v120, 16, v185
	v_lshlrev_b32_e32 v114, 16, v182
	v_and_b32_e32 v115, 0xffff0000, v182
	v_and_b32_e32 v121, 0xffff0000, v185
	v_pk_mul_f32 v[110:111], v[110:111], v[114:115]
	v_lshlrev_b32_e32 v116, 16, v183
	v_and_b32_e32 v117, 0xffff0000, v183
	v_pk_mul_f32 v[114:115], v[108:109], v[120:121]
	v_pk_mul_f32 v[108:109], v[106:107], v[118:119]
	v_cvt_pk_bf16_f32 v106, v110, v111
	v_add_co_u32_e32 v110, vcc, s4, v122
	v_pk_mul_f32 v[112:113], v[112:113], v[116:117]
	s_nop 0
	v_addc_co_u32_e32 v111, vcc, 0, v123, vcc
	v_cvt_pk_bf16_f32 v107, v112, v113
	v_cvt_pk_bf16_f32 v108, v108, v109
	v_cvt_pk_bf16_f32 v109, v114, v115
	global_store_dwordx4 v[110:111], v[106:109], off
	v_lshlrev_b32_e32 v112, 16, v180
	v_and_b32_e32 v113, 0xffff0000, v180
	v_lshlrev_b32_e32 v106, 16, v178
	v_and_b32_e32 v107, 0xffff0000, v178
	v_lshlrev_b32_e32 v108, 16, v179
	v_and_b32_e32 v109, 0xffff0000, v179
	v_lshlrev_b32_e32 v114, 16, v181
	v_and_b32_e32 v115, 0xffff0000, v181
	v_pk_mul_f32 v[104:105], v[104:105], v[108:109]
	v_pk_mul_f32 v[102:103], v[102:103], v[106:107]
	v_pk_mul_f32 v[106:107], v[100:101], v[114:115]
	v_pk_mul_f32 v[100:101], v[98:99], v[112:113]
	v_cvt_pk_bf16_f32 v98, v102, v103
	v_cvt_pk_bf16_f32 v99, v104, v105
	v_lshlrev_b32_e32 v102, 16, v176
	v_cvt_pk_bf16_f32 v100, v100, v101
	v_cvt_pk_bf16_f32 v101, v106, v107
	global_store_dwordx4 v[110:111], v[98:101], off offset:256
	v_and_b32_e32 v103, 0xffff0000, v176
	v_lshlrev_b32_e32 v104, 16, v177
	v_lshlrev_b32_e32 v98, 16, v174
	v_and_b32_e32 v99, 0xffff0000, v174
	v_and_b32_e32 v105, 0xffff0000, v177
	v_pk_mul_f32 v[94:95], v[94:95], v[98:99]
	v_lshlrev_b32_e32 v100, 16, v175
	v_and_b32_e32 v101, 0xffff0000, v175
	v_pk_mul_f32 v[98:99], v[92:93], v[104:105]
	v_pk_mul_f32 v[92:93], v[90:91], v[102:103]
	v_cvt_pk_bf16_f32 v90, v94, v95
	v_add_co_u32_e32 v94, vcc, s73, v122
	v_pk_mul_f32 v[96:97], v[96:97], v[100:101]
	s_nop 0
	v_addc_co_u32_e32 v95, vcc, 0, v123, vcc
	v_cvt_pk_bf16_f32 v91, v96, v97
	v_cvt_pk_bf16_f32 v92, v92, v93
	v_cvt_pk_bf16_f32 v93, v98, v99
	global_store_dwordx4 v[94:95], v[90:93], off
	v_lshlrev_b32_e32 v96, 16, v172
	v_and_b32_e32 v97, 0xffff0000, v172
	v_lshlrev_b32_e32 v90, 16, v170
	v_and_b32_e32 v91, 0xffff0000, v170
	v_lshlrev_b32_e32 v92, 16, v171
	v_and_b32_e32 v93, 0xffff0000, v171
	v_lshlrev_b32_e32 v98, 16, v173
	v_and_b32_e32 v99, 0xffff0000, v173
	v_pk_mul_f32 v[88:89], v[88:89], v[92:93]
	v_pk_mul_f32 v[86:87], v[86:87], v[90:91]
	v_pk_mul_f32 v[90:91], v[84:85], v[98:99]
	v_pk_mul_f32 v[84:85], v[82:83], v[96:97]
	v_cvt_pk_bf16_f32 v82, v86, v87
	v_cvt_pk_bf16_f32 v83, v88, v89
	v_lshlrev_b32_e32 v86, 16, v168
	v_cvt_pk_bf16_f32 v84, v84, v85
	v_cvt_pk_bf16_f32 v85, v90, v91
	global_store_dwordx4 v[94:95], v[82:85], off offset:256
	v_and_b32_e32 v87, 0xffff0000, v168
	v_lshlrev_b32_e32 v88, 16, v169
	v_lshlrev_b32_e32 v82, 16, v166
	v_and_b32_e32 v83, 0xffff0000, v166
	v_and_b32_e32 v89, 0xffff0000, v169
	v_pk_mul_f32 v[78:79], v[78:79], v[82:83]
	v_lshlrev_b32_e32 v84, 16, v167
	v_and_b32_e32 v85, 0xffff0000, v167
	v_pk_mul_f32 v[82:83], v[76:77], v[88:89]
	v_pk_mul_f32 v[76:77], v[74:75], v[86:87]
	v_cvt_pk_bf16_f32 v74, v78, v79
	v_add_co_u32_e32 v78, vcc, s5, v122
	v_pk_mul_f32 v[80:81], v[80:81], v[84:85]
	s_nop 0
	v_addc_co_u32_e32 v79, vcc, 0, v123, vcc
	v_cvt_pk_bf16_f32 v75, v80, v81
	v_cvt_pk_bf16_f32 v76, v76, v77
	v_cvt_pk_bf16_f32 v77, v82, v83
	global_store_dwordx4 v[78:79], v[74:77], off
	v_lshlrev_b32_e32 v80, 16, v164
	v_and_b32_e32 v81, 0xffff0000, v164
	v_lshlrev_b32_e32 v74, 16, v162
	v_and_b32_e32 v75, 0xffff0000, v162
	v_lshlrev_b32_e32 v76, 16, v163
	v_and_b32_e32 v77, 0xffff0000, v163
	v_lshlrev_b32_e32 v82, 16, v165
	v_and_b32_e32 v83, 0xffff0000, v165
	v_pk_mul_f32 v[72:73], v[72:73], v[76:77]
	v_pk_mul_f32 v[70:71], v[70:71], v[74:75]
	v_pk_mul_f32 v[74:75], v[68:69], v[82:83]
	v_pk_mul_f32 v[68:69], v[66:67], v[80:81]
	v_cvt_pk_bf16_f32 v66, v70, v71
	v_cvt_pk_bf16_f32 v67, v72, v73
	v_lshlrev_b32_e32 v70, 16, v160
	v_cvt_pk_bf16_f32 v68, v68, v69
	v_cvt_pk_bf16_f32 v69, v74, v75
	global_store_dwordx4 v[78:79], v[66:69], off offset:256
	v_and_b32_e32 v71, 0xffff0000, v160
	v_lshlrev_b32_e32 v72, 16, v161
	v_lshlrev_b32_e32 v66, 16, v158
	v_and_b32_e32 v67, 0xffff0000, v158
	v_and_b32_e32 v73, 0xffff0000, v161
	v_pk_mul_f32 v[62:63], v[62:63], v[66:67]
	v_lshlrev_b32_e32 v68, 16, v159
	v_and_b32_e32 v69, 0xffff0000, v159
	v_pk_mul_f32 v[66:67], v[60:61], v[72:73]
	v_pk_mul_f32 v[60:61], v[58:59], v[70:71]
	v_cvt_pk_bf16_f32 v58, v62, v63
	v_add_co_u32_e32 v62, vcc, s16, v122
	v_pk_mul_f32 v[64:65], v[64:65], v[68:69]
	s_nop 0
	v_addc_co_u32_e32 v63, vcc, 0, v123, vcc
	v_cvt_pk_bf16_f32 v59, v64, v65
	v_cvt_pk_bf16_f32 v60, v60, v61
	v_cvt_pk_bf16_f32 v61, v66, v67
	global_store_dwordx4 v[62:63], v[58:61], off
	v_lshlrev_b32_e32 v64, 16, v156
	v_and_b32_e32 v65, 0xffff0000, v156
	v_lshlrev_b32_e32 v58, 16, v154
	v_and_b32_e32 v59, 0xffff0000, v154
	v_lshlrev_b32_e32 v60, 16, v155
	v_and_b32_e32 v61, 0xffff0000, v155
	v_lshlrev_b32_e32 v66, 16, v157
	v_and_b32_e32 v67, 0xffff0000, v157
	v_pk_mul_f32 v[56:57], v[56:57], v[60:61]
	v_pk_mul_f32 v[54:55], v[54:55], v[58:59]
	v_pk_mul_f32 v[58:59], v[52:53], v[66:67]
	v_pk_mul_f32 v[52:53], v[50:51], v[64:65]
	v_cvt_pk_bf16_f32 v50, v54, v55
	v_cvt_pk_bf16_f32 v51, v56, v57
	v_lshlrev_b32_e32 v54, 16, v152
	v_cvt_pk_bf16_f32 v52, v52, v53
	v_cvt_pk_bf16_f32 v53, v58, v59
	global_store_dwordx4 v[62:63], v[50:53], off offset:256
	v_and_b32_e32 v55, 0xffff0000, v152
	v_lshlrev_b32_e32 v56, 16, v153
	v_lshlrev_b32_e32 v50, 16, v150
	v_and_b32_e32 v51, 0xffff0000, v150
	v_and_b32_e32 v57, 0xffff0000, v153
	v_pk_mul_f32 v[46:47], v[46:47], v[50:51]
	v_lshlrev_b32_e32 v52, 16, v151
	v_and_b32_e32 v53, 0xffff0000, v151
	v_pk_mul_f32 v[50:51], v[44:45], v[56:57]
	v_pk_mul_f32 v[44:45], v[42:43], v[54:55]
	v_cvt_pk_bf16_f32 v42, v46, v47
	v_add_co_u32_e32 v46, vcc, s18, v122
	v_pk_mul_f32 v[48:49], v[48:49], v[52:53]
	s_nop 0
	v_addc_co_u32_e32 v47, vcc, 0, v123, vcc
	v_cvt_pk_bf16_f32 v43, v48, v49
	v_cvt_pk_bf16_f32 v44, v44, v45
	v_cvt_pk_bf16_f32 v45, v50, v51
	global_store_dwordx4 v[46:47], v[42:45], off
	v_lshlrev_b32_e32 v48, 16, v148
	v_and_b32_e32 v49, 0xffff0000, v148
	v_lshlrev_b32_e32 v42, 16, v146
	v_and_b32_e32 v43, 0xffff0000, v146
	v_lshlrev_b32_e32 v44, 16, v147
	v_and_b32_e32 v45, 0xffff0000, v147
	v_lshlrev_b32_e32 v50, 16, v149
	v_and_b32_e32 v51, 0xffff0000, v149
	v_pk_mul_f32 v[40:41], v[40:41], v[44:45]
	v_pk_mul_f32 v[38:39], v[38:39], v[42:43]
	v_pk_mul_f32 v[42:43], v[36:37], v[50:51]
	v_pk_mul_f32 v[36:37], v[34:35], v[48:49]
	v_cvt_pk_bf16_f32 v34, v38, v39
	v_cvt_pk_bf16_f32 v35, v40, v41
	v_lshlrev_b32_e32 v38, 16, v144
	v_cvt_pk_bf16_f32 v36, v36, v37
	v_cvt_pk_bf16_f32 v37, v42, v43
	global_store_dwordx4 v[46:47], v[34:37], off offset:256
	v_and_b32_e32 v39, 0xffff0000, v144
	v_lshlrev_b32_e32 v40, 16, v145
	v_lshlrev_b32_e32 v34, 16, v142
	v_and_b32_e32 v35, 0xffff0000, v142
	v_and_b32_e32 v41, 0xffff0000, v145
	v_pk_mul_f32 v[30:31], v[30:31], v[34:35]
	v_lshlrev_b32_e32 v36, 16, v143
	v_and_b32_e32 v37, 0xffff0000, v143
	v_pk_mul_f32 v[34:35], v[28:29], v[40:41]
	v_pk_mul_f32 v[28:29], v[26:27], v[38:39]
	v_cvt_pk_bf16_f32 v26, v30, v31
	v_add_co_u32_e32 v30, vcc, s17, v122
	v_pk_mul_f32 v[32:33], v[32:33], v[36:37]
	s_nop 0
	v_addc_co_u32_e32 v31, vcc, 0, v123, vcc
	v_cvt_pk_bf16_f32 v27, v32, v33
	v_cvt_pk_bf16_f32 v28, v28, v29
	v_cvt_pk_bf16_f32 v29, v34, v35
	global_store_dwordx4 v[30:31], v[26:29], off
	v_lshlrev_b32_e32 v32, 16, v140
	v_and_b32_e32 v33, 0xffff0000, v140
	v_lshlrev_b32_e32 v26, 16, v138
	v_and_b32_e32 v27, 0xffff0000, v138
	v_lshlrev_b32_e32 v28, 16, v139
	v_and_b32_e32 v29, 0xffff0000, v139
	v_lshlrev_b32_e32 v34, 16, v141
	v_and_b32_e32 v35, 0xffff0000, v141
	v_pk_mul_f32 v[24:25], v[24:25], v[28:29]
	v_pk_mul_f32 v[22:23], v[22:23], v[26:27]
	v_pk_mul_f32 v[26:27], v[20:21], v[34:35]
	v_pk_mul_f32 v[20:21], v[18:19], v[32:33]
	v_cvt_pk_bf16_f32 v18, v22, v23
	v_cvt_pk_bf16_f32 v19, v24, v25
	v_lshlrev_b32_e32 v22, 16, v136
	v_cvt_pk_bf16_f32 v20, v20, v21
	v_cvt_pk_bf16_f32 v21, v26, v27
	global_store_dwordx4 v[30:31], v[18:21], off offset:256
	v_and_b32_e32 v23, 0xffff0000, v136
	v_lshlrev_b32_e32 v24, 16, v137
	v_lshlrev_b32_e32 v18, 16, v134
	v_and_b32_e32 v19, 0xffff0000, v134
	v_and_b32_e32 v25, 0xffff0000, v137
	v_pk_mul_f32 v[14:15], v[14:15], v[18:19]
	v_lshlrev_b32_e32 v20, 16, v135
	v_and_b32_e32 v21, 0xffff0000, v135
	v_pk_mul_f32 v[18:19], v[12:13], v[24:25]
	v_pk_mul_f32 v[12:13], v[10:11], v[22:23]
	v_cvt_pk_bf16_f32 v10, v14, v15
	v_add_co_u32_e32 v14, vcc, s95, v122
	v_pk_mul_f32 v[16:17], v[16:17], v[20:21]
	s_nop 0
	v_addc_co_u32_e32 v15, vcc, 0, v123, vcc
	v_cvt_pk_bf16_f32 v11, v16, v17
	v_cvt_pk_bf16_f32 v12, v12, v13
	v_cvt_pk_bf16_f32 v13, v18, v19
	global_store_dwordx4 v[14:15], v[10:13], off
	v_lshlrev_b32_e32 v16, 16, v132
	v_and_b32_e32 v17, 0xffff0000, v132
	v_lshlrev_b32_e32 v10, 16, v130
	v_and_b32_e32 v11, 0xffff0000, v130
	v_lshlrev_b32_e32 v18, 16, v133
	v_and_b32_e32 v19, 0xffff0000, v133
	v_lshlrev_b32_e32 v12, 16, v131
	v_and_b32_e32 v13, 0xffff0000, v131
	v_pk_mul_f32 v[6:7], v[6:7], v[10:11]
	v_pk_mul_f32 v[10:11], v[4:5], v[18:19]
	v_pk_mul_f32 v[4:5], v[2:3], v[16:17]
	s_mov_b64 s[4:5], -1
	s_and_b64 vcc, exec, s[2:3]
	v_pk_mul_f32 v[8:9], v[8:9], v[12:13]
	v_cvt_pk_bf16_f32 v2, v6, v7
	s_nop 0
	v_cvt_pk_bf16_f32 v3, v8, v9
	v_cvt_pk_bf16_f32 v4, v4, v5
	v_cvt_pk_bf16_f32 v5, v10, v11
	global_store_dwordx4 v[14:15], v[2:5], off offset:256
	s_cbranch_vccnz .LBB0_566
	s_andn2_b64 vcc, exec, s[8:9]
	s_cbranch_vccnz .LBB0_565
	s_mov_b32 s101, 1
	s_branch .LBB0_565

.LBB0_660:
	s_mov_b64 s[22:23], 0
	s_add_u32 s0, s0, s22
	s_addc_u32 s1, s1, s23
	s_add_u32 s4, s4, s22
	s_addc_u32 s5, s5, s23
	s_mov_b32 s52, 16
	s_cmp_lt_i32 s52, 1
	s_cbranch_scc1 .LBB0_671
	s_ashr_i32 s19, s18, 31
	s_lshl_b64 s[22:23], s[18:19], 19
	s_add_u32 s19, s27, s22
	s_addc_u32 s53, s28, s23
	s_ashr_i32 s17, s16, 31
	s_lshl_b64 s[22:23], s[16:17], 19
	s_add_u32 s17, s29, s22
	s_addc_u32 s54, s30, s23
	s_mov_b32 s55, 2
	s_mov_b64 s[22:23], 0x40080
	s_cmp_lg_u32 s101, 0
	s_cbranch_scc0 .Lrob_5
	s_barrier
	s_mov_b32 s101, 0

.LBB0_668:
	s_andn2_b64 vcc, exec, s[2:3]
	s_mov_b64 s[2:3], -1
	s_cbranch_vccnz .LBB0_653
	s_andn2_b64 vcc, exec, s[6:7]
	s_cbranch_vccnz .LBB0_652
	s_mov_b32 s101, 1
	s_branch .LBB0_652

.LBB0_959:
	s_add_u32 s20, s20, s24
	s_addc_u32 s21, s21, s25
	s_mov_b32 s19, 8
	s_cmp_lt_i32 s19, 1
	s_cbranch_scc1 .LBB0_965
	s_and_b64 s[24:25], exec, s[4:5]
	s_cselect_b32 s25, s21, s7
	s_cselect_b32 s24, s20, s6
	s_mov_b32 s60, 2
	s_mov_b64 s[26:27], 0x80
	s_cmp_lg_u32 s101, 0
	s_cbranch_scc0 .Lrob_6
	s_barrier
	s_mov_b32 s101, 0

.LBB0_968:
	s_mov_b32 s5, 0xbc800000
	v_mul_f32_e32 v4, s5, v146
	v_mul_f32_e32 v5, s5, v147
	v_mul_f32_e32 v6, s5, v148
	v_mul_f32_e32 v7, s5, v149
	v_mul_f32_e32 v8, s5, v158
	v_mul_f32_e32 v9, s5, v159
	v_mul_f32_e32 v10, s5, v160
	v_mul_f32_e32 v11, s5, v161
	s_mov_b32 s19, 0x45800000
	v_exp_f32_e32 v4, v4
	v_exp_f32_e32 v5, v5
	v_exp_f32_e32 v12, v6
	v_exp_f32_e32 v7, v7
	v_exp_f32_e32 v8, v8
	v_exp_f32_e32 v9, v9
	v_exp_f32_e32 v10, v10
	v_exp_f32_e32 v11, v11
	s_nop 0
	v_fma_f32 v4, v4, s19, s19
	v_fma_f32 v5, v5, s19, s19
	v_fma_f32 v12, v12, s19, s19
	v_fma_f32 v7, v7, s19, s19
	v_fma_f32 v8, v8, s19, s19
	v_fma_f32 v9, v9, s19, s19
	v_fma_f32 v10, v10, s19, s19
	v_fma_f32 v11, v11, s19, s19
	v_mul_f32_e32 v13, v146, v154
	v_mul_f32_e32 v14, v147, v155
	v_mul_f32_e32 v15, v148, v156
	v_mul_f32_e32 v16, v149, v157
	v_mul_f32_e32 v17, v158, v150
	v_mul_f32_e32 v18, v159, v151
	v_mul_f32_e32 v19, v160, v152
	v_mul_f32_e32 v20, v161, v153
	v_mov_b32_e32 v24, 0x43e00000
	v_rcp_f32_e32 v4, v4
	v_rcp_f32_e32 v5, v5
	v_rcp_f32_e32 v12, v12
	v_rcp_f32_e32 v8, v8
	v_rcp_f32_e32 v9, v9
	v_rcp_f32_e32 v11, v11
	v_mov_b32_e32 v2, v0
	v_rcp_f32_e32 v7, v7
	v_rcp_f32_e32 v10, v10
	s_nop 0
	v_mul_f32_e32 v13, v13, v4
	v_mul_f32_e32 v14, v14, v5
	v_mul_f32_e32 v15, v15, v12
	v_mul_f32_e32 v16, v16, v7
	v_mul_f32_e32 v17, v17, v8
	v_mul_f32_e32 v18, v18, v9
	v_mul_f32_e32 v19, v19, v10
	v_mul_f32_e32 v20, v20, v11
	v_mov_b32_e32 v8, v195
	v_med3_f32 v4, v13, s35, v24
	v_med3_f32 v5, v14, s35, v24
	v_med3_f32 v11, v17, s35, v24
	v_med3_f32 v12, v18, s35, v24
	v_mov_b32_e32 v9, v195
	v_cvt_pk_fp8_f32 v8, v4, v5
	v_ashrrev_i32_e32 v3, 2, v2
	v_cvt_pk_fp8_f32 v9, v11, v12
	v_and_b32_e32 v3, 0xffffffc0, v3
	v_lshl_add_u32 v3, s55, 8, v3
	v_and_or_b32 v6, v2, 15, v3
	v_lshrrev_b32_e32 v2, 1, v2
	v_med3_f32 v7, v15, s35, v24
	v_med3_f32 v10, v16, s35, v24
	v_med3_f32 v4, v19, s35, v24
	v_med3_f32 v5, v20, s35, v24
	v_and_b32_e32 v2, 0x78, v2
	v_cvt_pk_fp8_f32 v8, v7, v10 op_sel:[0,0,1]
	v_cvt_pk_fp8_f32 v9, v4, v5 op_sel:[0,0,1]
	v_mul_f32_e32 v4, s5, v142
	v_mul_f32_e32 v5, s5, v143
	v_mul_f32_e32 v7, s5, v144
	v_mul_f32_e32 v10, s5, v145
	v_mul_f32_e32 v11, s5, v138
	v_mul_f32_e32 v12, s5, v139
	v_mul_f32_e32 v13, s5, v140
	v_mul_f32_e32 v14, s5, v141
	v_lshl_or_b32 v2, s59, 7, v2
	v_exp_f32_e32 v15, v4
	v_exp_f32_e32 v16, v5
	v_mov_b64_e32 v[4:5], s[14:15]
	s_movk_i32 s4, 0xb00
	v_ashrrev_i32_e32 v3, 31, v2
	v_exp_f32_e32 v17, v10
	v_exp_f32_e32 v18, v11
	v_mad_i64_i32 v[10:11], s[0:1], v6, s4, v[4:5]
	v_exp_f32_e32 v7, v7
	v_exp_f32_e32 v12, v12
	v_exp_f32_e32 v13, v13
	v_exp_f32_e32 v14, v14
	v_lshl_add_u64 v[10:11], v[10:11], 0, v[2:3]
	s_nop 0
	v_fma_f32 v15, v15, s19, s19
	v_fma_f32 v16, v16, s19, s19
	v_fma_f32 v7, v7, s19, s19
	v_fma_f32 v17, v17, s19, s19
	v_fma_f32 v18, v18, s19, s19
	v_fma_f32 v12, v12, s19, s19
	v_fma_f32 v13, v13, s19, s19
	v_fma_f32 v14, v14, s19, s19
	global_store_dwordx2 v[10:11], v[8:9], off
	v_mul_f32_e32 v8, v142, v134
	v_mul_f32_e32 v9, v143, v135
	v_mul_f32_e32 v10, v144, v136
	v_mul_f32_e32 v11, v145, v137
	v_mul_f32_e32 v19, v138, v130
	v_mul_f32_e32 v20, v139, v131
	v_mul_f32_e32 v21, v140, v132
	v_mul_f32_e32 v22, v141, v133
	v_rcp_f32_e32 v15, v15
	v_rcp_f32_e32 v16, v16
	v_rcp_f32_e32 v7, v7
	v_rcp_f32_e32 v17, v17
	v_rcp_f32_e32 v18, v18
	v_rcp_f32_e32 v12, v12
	v_rcp_f32_e32 v13, v13
	v_rcp_f32_e32 v14, v14
	s_nop 0
	v_mul_f32_e32 v8, v8, v15
	v_mul_f32_e32 v9, v9, v16
	v_mul_f32_e32 v10, v10, v7
	v_mul_f32_e32 v11, v11, v17
	v_mul_f32_e32 v19, v19, v18
	v_mul_f32_e32 v20, v20, v12
	v_mul_f32_e32 v21, v21, v13
	v_mul_f32_e32 v22, v22, v14
	s_and_b64 vcc, exec, s[2:3]
	v_med3_f32 v7, v8, s35, v24
	v_med3_f32 v9, v9, s35, v24
	v_mov_b32_e32 v8, v195
	v_med3_f32 v12, v19, s35, v24
	v_med3_f32 v13, v20, s35, v24
	v_cvt_pk_fp8_f32 v8, v7, v9
	v_mov_b32_e32 v9, v195
	v_cvt_pk_fp8_f32 v9, v12, v13
	v_med3_f32 v10, v10, s35, v24
	v_med3_f32 v11, v11, s35, v24
	v_med3_f32 v7, v21, s35, v24
	v_med3_f32 v12, v22, s35, v24
	v_cvt_pk_fp8_f32 v8, v10, v11 op_sel:[0,0,1]
	v_cvt_pk_fp8_f32 v9, v7, v12 op_sel:[0,0,1]
	v_mul_f32_e32 v7, s5, v126
	v_mul_f32_e32 v10, s5, v127
	v_mul_f32_e32 v11, s5, v128
	v_mul_f32_e32 v12, s5, v129
	v_mul_f32_e32 v13, s5, v122
	v_mul_f32_e32 v14, s5, v123
	v_mul_f32_e32 v15, s5, v124
	v_mul_f32_e32 v16, s5, v125
	s_nop 0
	v_exp_f32_e32 v17, v10
	v_or_b32_e32 v10, 16, v6
	v_exp_f32_e32 v18, v11
	v_mad_i64_i32 v[10:11], s[0:1], v10, s4, v[4:5]
	v_exp_f32_e32 v7, v7
	v_exp_f32_e32 v12, v12
	v_exp_f32_e32 v13, v13
	v_exp_f32_e32 v14, v14
	v_exp_f32_e32 v15, v15
	v_exp_f32_e32 v16, v16
	v_lshl_add_u64 v[10:11], v[10:11], 0, v[2:3]
	s_nop 0
	v_fma_f32 v7, v7, s19, s19
	v_fma_f32 v17, v17, s19, s19
	v_fma_f32 v18, v18, s19, s19
	v_fma_f32 v12, v12, s19, s19
	v_fma_f32 v13, v13, s19, s19
	v_fma_f32 v14, v14, s19, s19
	v_fma_f32 v15, v15, s19, s19
	v_fma_f32 v16, v16, s19, s19
	global_store_dwordx2 v[10:11], v[8:9], off
	v_mul_f32_e32 v8, v126, v118
	v_mul_f32_e32 v9, v127, v119
	v_mul_f32_e32 v10, v128, v120
	v_mul_f32_e32 v11, v129, v121
	v_mul_f32_e32 v19, v122, v114
	v_mul_f32_e32 v20, v123, v115
	v_mul_f32_e32 v21, v124, v116
	v_mul_f32_e32 v22, v125, v117
	v_rcp_f32_e32 v7, v7
	v_rcp_f32_e32 v17, v17
	v_rcp_f32_e32 v18, v18
	v_rcp_f32_e32 v12, v12
	v_rcp_f32_e32 v13, v13
	v_rcp_f32_e32 v14, v14
	v_rcp_f32_e32 v15, v15
	v_rcp_f32_e32 v16, v16
	s_nop 0
	v_mul_f32_e32 v8, v8, v7
	v_mul_f32_e32 v9, v9, v17
	v_mul_f32_e32 v10, v10, v18
	v_mul_f32_e32 v11, v11, v12
	v_mul_f32_e32 v19, v19, v13
	v_mul_f32_e32 v20, v20, v14
	v_mul_f32_e32 v21, v21, v15
	v_mul_f32_e32 v22, v22, v16
	s_nop 0
	v_med3_f32 v7, v8, s35, v24
	v_med3_f32 v9, v9, s35, v24
	v_mov_b32_e32 v8, v195
	v_med3_f32 v12, v19, s35, v24
	v_med3_f32 v13, v20, s35, v24
	v_cvt_pk_fp8_f32 v8, v7, v9
	v_mov_b32_e32 v9, v195
	v_cvt_pk_fp8_f32 v9, v12, v13
	v_med3_f32 v10, v10, s35, v24
	v_med3_f32 v11, v11, s35, v24
	v_med3_f32 v7, v21, s35, v24
	v_med3_f32 v12, v22, s35, v24
	v_cvt_pk_fp8_f32 v8, v10, v11 op_sel:[0,0,1]
	v_cvt_pk_fp8_f32 v9, v7, v12 op_sel:[0,0,1]
	v_mul_f32_e32 v7, s5, v110
	v_mul_f32_e32 v10, s5, v111
	v_mul_f32_e32 v11, s5, v112
	v_mul_f32_e32 v12, s5, v113
	v_mul_f32_e32 v13, s5, v106
	v_mul_f32_e32 v14, s5, v107
	v_mul_f32_e32 v15, s5, v108
	v_mul_f32_e32 v16, s5, v109
	s_nop 0
	v_exp_f32_e32 v17, v10
	v_or_b32_e32 v10, 32, v6
	v_exp_f32_e32 v18, v11
	v_mad_i64_i32 v[10:11], s[0:1], v10, s4, v[4:5]
	v_exp_f32_e32 v7, v7
	v_exp_f32_e32 v12, v12
	v_exp_f32_e32 v13, v13
	v_exp_f32_e32 v14, v14
	v_exp_f32_e32 v15, v15
	v_exp_f32_e32 v16, v16
	v_lshl_add_u64 v[10:11], v[10:11], 0, v[2:3]
	s_nop 0
	v_fma_f32 v7, v7, s19, s19
	v_fma_f32 v17, v17, s19, s19
	v_fma_f32 v18, v18, s19, s19
	v_fma_f32 v12, v12, s19, s19
	v_fma_f32 v13, v13, s19, s19
	v_fma_f32 v14, v14, s19, s19
	v_fma_f32 v15, v15, s19, s19
	v_fma_f32 v16, v16, s19, s19
	global_store_dwordx2 v[10:11], v[8:9], off
	v_mul_f32_e32 v8, v110, v102
	v_mul_f32_e32 v9, v111, v103
	v_mul_f32_e32 v10, v112, v104
	v_mul_f32_e32 v11, v113, v105
	v_mul_f32_e32 v19, v106, v98
	v_mul_f32_e32 v20, v107, v99
	v_mul_f32_e32 v21, v108, v100
	v_mul_f32_e32 v22, v109, v101
	v_rcp_f32_e32 v7, v7
	v_rcp_f32_e32 v17, v17
	v_rcp_f32_e32 v18, v18
	v_rcp_f32_e32 v12, v12
	v_rcp_f32_e32 v13, v13
	v_rcp_f32_e32 v14, v14
	v_rcp_f32_e32 v15, v15
	v_rcp_f32_e32 v16, v16
	s_nop 0
	v_mul_f32_e32 v8, v8, v7
	v_mul_f32_e32 v9, v9, v17
	v_mul_f32_e32 v10, v10, v18
	v_mul_f32_e32 v11, v11, v12
	v_mul_f32_e32 v19, v19, v13
	v_mul_f32_e32 v20, v20, v14
	v_mul_f32_e32 v21, v21, v15
	v_mul_f32_e32 v22, v22, v16
	s_nop 0
	v_med3_f32 v7, v8, s35, v24
	v_med3_f32 v9, v9, s35, v24
	v_mov_b32_e32 v8, v195
	v_med3_f32 v12, v19, s35, v24
	v_med3_f32 v13, v20, s35, v24
	v_cvt_pk_fp8_f32 v8, v7, v9
	v_mov_b32_e32 v9, v195
	v_cvt_pk_fp8_f32 v9, v12, v13
	v_med3_f32 v10, v10, s35, v24
	v_med3_f32 v11, v11, s35, v24
	v_med3_f32 v7, v21, s35, v24
	v_med3_f32 v12, v22, s35, v24
	v_cvt_pk_fp8_f32 v8, v10, v11 op_sel:[0,0,1]
	v_cvt_pk_fp8_f32 v9, v7, v12 op_sel:[0,0,1]
	v_or_b32_e32 v7, 48, v6
	v_mul_f32_e32 v10, s5, v94
	v_mul_f32_e32 v11, s5, v95
	v_mul_f32_e32 v12, s5, v96
	v_mul_f32_e32 v13, s5, v97
	v_mul_f32_e32 v14, s5, v90
	v_mul_f32_e32 v15, s5, v91
	v_mul_f32_e32 v16, s5, v92
	v_mul_f32_e32 v17, s5, v93
	s_nop 0
	v_exp_f32_e32 v18, v10
	v_exp_f32_e32 v19, v11
	v_exp_f32_e32 v12, v12
	v_exp_f32_e32 v13, v13
	v_exp_f32_e32 v14, v14
	v_exp_f32_e32 v15, v15
	v_exp_f32_e32 v16, v16
	v_exp_f32_e32 v17, v17
	v_mad_i64_i32 v[10:11], s[0:1], v7, s4, v[4:5]
	v_lshl_add_u64 v[10:11], v[10:11], 0, v[2:3]
	s_nop 0
	v_fma_f32 v18, v18, s19, s19
	v_fma_f32 v19, v19, s19, s19
	v_fma_f32 v12, v12, s19, s19
	v_fma_f32 v13, v13, s19, s19
	v_fma_f32 v14, v14, s19, s19
	v_fma_f32 v15, v15, s19, s19
	v_fma_f32 v16, v16, s19, s19
	v_fma_f32 v17, v17, s19, s19
	global_store_dwordx2 v[10:11], v[8:9], off
	v_rcp_f32_e32 v7, v18
	v_rcp_f32_e32 v18, v19
	v_mul_f32_e32 v8, v94, v86
	v_mul_f32_e32 v9, v95, v87
	v_mul_f32_e32 v11, v96, v88
	v_mul_f32_e32 v19, v97, v89
	v_mul_f32_e32 v20, v90, v82
	v_mul_f32_e32 v21, v91, v83
	v_mul_f32_e32 v22, v92, v84
	v_mul_f32_e32 v23, v93, v85
	v_rcp_f32_e32 v12, v12
	v_rcp_f32_e32 v13, v13
	v_rcp_f32_e32 v14, v14
	v_rcp_f32_e32 v15, v15
	v_rcp_f32_e32 v16, v16
	v_rcp_f32_e32 v17, v17
	s_nop 0
	v_mul_f32_e32 v8, v8, v7
	v_mul_f32_e32 v9, v9, v18
	v_mul_f32_e32 v11, v11, v12
	v_mul_f32_e32 v19, v19, v13
	v_mul_f32_e32 v20, v20, v14
	v_mul_f32_e32 v21, v21, v15
	v_mul_f32_e32 v22, v22, v16
	v_mul_f32_e32 v23, v23, v17
	v_add_u32_e32 v10, 0x80, v6
	v_med3_f32 v7, v8, s35, v24
	v_med3_f32 v9, v9, s35, v24
	v_mov_b32_e32 v8, v195
	v_med3_f32 v13, v20, s35, v24
	v_cvt_pk_fp8_f32 v8, v7, v9
	v_med3_f32 v7, v21, s35, v24
	v_mov_b32_e32 v9, v195
	v_cvt_pk_fp8_f32 v9, v13, v7
	v_med3_f32 v11, v11, s35, v24
	v_med3_f32 v12, v19, s35, v24
	v_med3_f32 v14, v22, s35, v24
	v_med3_f32 v15, v23, s35, v24
	v_cvt_pk_fp8_f32 v8, v11, v12 op_sel:[0,0,1]
	v_cvt_pk_fp8_f32 v9, v14, v15 op_sel:[0,0,1]
	v_mul_f32_e32 v7, s5, v78
	v_mul_f32_e32 v11, s5, v79
	v_mul_f32_e32 v12, s5, v80
	v_mul_f32_e32 v13, s5, v81
	v_mul_f32_e32 v16, s5, v74
	v_mul_f32_e32 v17, s5, v75
	v_mul_f32_e32 v18, s5, v76
	v_mul_f32_e32 v19, s5, v77
	s_nop 0
	v_exp_f32_e32 v7, v7
	v_exp_f32_e32 v20, v11
	v_exp_f32_e32 v12, v12
	v_exp_f32_e32 v13, v13
	v_exp_f32_e32 v16, v16
	v_exp_f32_e32 v17, v17
	v_exp_f32_e32 v18, v18
	v_exp_f32_e32 v19, v19
	v_mad_i64_i32 v[10:11], s[0:1], v10, s4, v[4:5]
	s_nop 0
	v_fma_f32 v7, v7, s19, s19
	v_fma_f32 v20, v20, s19, s19
	v_fma_f32 v12, v12, s19, s19
	v_fma_f32 v13, v13, s19, s19
	v_fma_f32 v16, v16, s19, s19
	v_fma_f32 v17, v17, s19, s19
	v_fma_f32 v18, v18, s19, s19
	v_fma_f32 v19, v19, s19, s19
	v_lshl_add_u64 v[10:11], v[10:11], 0, v[2:3]
	v_rcp_f32_e32 v14, v20
	v_rcp_f32_e32 v15, v16
	v_rcp_f32_e32 v16, v17
	v_rcp_f32_e32 v17, v18
	v_rcp_f32_e32 v18, v19
	global_store_dwordx2 v[10:11], v[8:9], off
	v_mul_f32_e32 v8, v78, v70
	v_mul_f32_e32 v9, v79, v71
	v_mul_f32_e32 v10, v80, v72
	v_mul_f32_e32 v11, v81, v73
	v_mul_f32_e32 v19, v74, v66
	v_mul_f32_e32 v20, v75, v67
	v_mul_f32_e32 v21, v76, v68
	v_mul_f32_e32 v22, v77, v69
	v_rcp_f32_e32 v7, v7
	v_rcp_f32_e32 v12, v12
	v_rcp_f32_e32 v13, v13
	s_nop 0
	v_mul_f32_e32 v8, v8, v7
	v_mul_f32_e32 v9, v9, v14
	v_mul_f32_e32 v10, v10, v12
	v_mul_f32_e32 v11, v11, v13
	v_mul_f32_e32 v19, v19, v15
	v_mul_f32_e32 v20, v20, v16
	v_mul_f32_e32 v21, v21, v17
	v_mul_f32_e32 v22, v22, v18
	s_nop 0
	v_med3_f32 v7, v8, s35, v24
	v_med3_f32 v9, v9, s35, v24
	v_mov_b32_e32 v8, v195
	v_med3_f32 v12, v19, s35, v24
	v_med3_f32 v13, v20, s35, v24
	v_cvt_pk_fp8_f32 v8, v7, v9
	v_mov_b32_e32 v9, v195
	v_cvt_pk_fp8_f32 v9, v12, v13
	v_med3_f32 v10, v10, s35, v24
	v_med3_f32 v11, v11, s35, v24
	v_med3_f32 v7, v21, s35, v24
	v_med3_f32 v12, v22, s35, v24
	v_cvt_pk_fp8_f32 v8, v10, v11 op_sel:[0,0,1]
	v_cvt_pk_fp8_f32 v9, v7, v12 op_sel:[0,0,1]
	v_mul_f32_e32 v7, s5, v62
	v_mul_f32_e32 v10, s5, v63
	v_mul_f32_e32 v11, s5, v64
	v_mul_f32_e32 v12, s5, v65
	v_mul_f32_e32 v13, s5, v58
	v_mul_f32_e32 v14, s5, v59
	v_mul_f32_e32 v15, s5, v60
	v_mul_f32_e32 v16, s5, v61
	s_nop 0
	v_exp_f32_e32 v17, v10
	v_add_u32_e32 v10, 0x90, v6
	v_exp_f32_e32 v18, v11
	v_mad_i64_i32 v[10:11], s[0:1], v10, s4, v[4:5]
	v_exp_f32_e32 v7, v7
	v_exp_f32_e32 v12, v12
	v_exp_f32_e32 v13, v13
	v_exp_f32_e32 v14, v14
	v_exp_f32_e32 v15, v15
	v_exp_f32_e32 v16, v16
	v_lshl_add_u64 v[10:11], v[10:11], 0, v[2:3]
	s_nop 0
	v_fma_f32 v7, v7, s19, s19
	v_fma_f32 v17, v17, s19, s19
	v_fma_f32 v18, v18, s19, s19
	v_fma_f32 v12, v12, s19, s19
	v_fma_f32 v13, v13, s19, s19
	v_fma_f32 v14, v14, s19, s19
	v_fma_f32 v15, v15, s19, s19
	v_fma_f32 v16, v16, s19, s19
	global_store_dwordx2 v[10:11], v[8:9], off
	v_mul_f32_e32 v8, v62, v54
	v_mul_f32_e32 v9, v63, v55
	v_mul_f32_e32 v10, v64, v56
	v_mul_f32_e32 v11, v65, v57
	v_mul_f32_e32 v19, v58, v50
	v_mul_f32_e32 v20, v59, v51
	v_mul_f32_e32 v21, v60, v52
	v_mul_f32_e32 v22, v61, v53
	v_rcp_f32_e32 v7, v7
	v_rcp_f32_e32 v17, v17
	v_rcp_f32_e32 v18, v18
	v_rcp_f32_e32 v12, v12
	v_rcp_f32_e32 v13, v13
	v_rcp_f32_e32 v14, v14
	v_rcp_f32_e32 v15, v15
	v_rcp_f32_e32 v16, v16
	s_nop 0
	v_mul_f32_e32 v8, v8, v7
	v_mul_f32_e32 v9, v9, v17
	v_mul_f32_e32 v10, v10, v18
	v_mul_f32_e32 v11, v11, v12
	v_mul_f32_e32 v19, v19, v13
	v_mul_f32_e32 v20, v20, v14
	v_mul_f32_e32 v21, v21, v15
	v_mul_f32_e32 v22, v22, v16
	s_nop 0
	v_med3_f32 v7, v8, s35, v24
	v_med3_f32 v9, v9, s35, v24
	v_mov_b32_e32 v8, v195
	v_med3_f32 v12, v19, s35, v24
	v_med3_f32 v13, v20, s35, v24
	v_cvt_pk_fp8_f32 v8, v7, v9
	v_mov_b32_e32 v9, v195
	v_cvt_pk_fp8_f32 v9, v12, v13
	v_med3_f32 v10, v10, s35, v24
	v_med3_f32 v11, v11, s35, v24
	v_med3_f32 v7, v21, s35, v24
	v_med3_f32 v12, v22, s35, v24
	v_cvt_pk_fp8_f32 v8, v10, v11 op_sel:[0,0,1]
	v_cvt_pk_fp8_f32 v9, v7, v12 op_sel:[0,0,1]
	v_mul_f32_e32 v7, s5, v46
	v_mul_f32_e32 v10, s5, v47
	v_mul_f32_e32 v11, s5, v48
	v_mul_f32_e32 v12, s5, v49
	v_mul_f32_e32 v13, s5, v42
	v_mul_f32_e32 v14, s5, v43
	v_mul_f32_e32 v15, s5, v44
	v_mul_f32_e32 v16, s5, v45
	s_nop 0
	v_exp_f32_e32 v17, v10
	v_add_u32_e32 v10, 0xa0, v6
	v_exp_f32_e32 v18, v11
	v_mad_i64_i32 v[10:11], s[0:1], v10, s4, v[4:5]
	v_exp_f32_e32 v7, v7
	v_exp_f32_e32 v12, v12
	v_exp_f32_e32 v13, v13
	v_exp_f32_e32 v14, v14
	v_exp_f32_e32 v15, v15
	v_exp_f32_e32 v16, v16
	v_lshl_add_u64 v[10:11], v[10:11], 0, v[2:3]
	s_nop 0
	v_fma_f32 v7, v7, s19, s19
	v_fma_f32 v17, v17, s19, s19
	v_fma_f32 v18, v18, s19, s19
	v_fma_f32 v12, v12, s19, s19
	v_fma_f32 v13, v13, s19, s19
	v_fma_f32 v14, v14, s19, s19
	v_fma_f32 v15, v15, s19, s19
	v_fma_f32 v16, v16, s19, s19
	global_store_dwordx2 v[10:11], v[8:9], off
	v_mul_f32_e32 v8, v46, v38
	v_mul_f32_e32 v9, v47, v39
	v_mul_f32_e32 v10, v48, v40
	v_mul_f32_e32 v11, v49, v41
	v_mul_f32_e32 v19, v42, v34
	v_mul_f32_e32 v20, v43, v35
	v_mul_f32_e32 v21, v44, v36
	v_mul_f32_e32 v22, v45, v37
	v_rcp_f32_e32 v7, v7
	v_rcp_f32_e32 v17, v17
	v_rcp_f32_e32 v18, v18
	v_rcp_f32_e32 v12, v12
	v_rcp_f32_e32 v13, v13
	v_rcp_f32_e32 v14, v14
	v_rcp_f32_e32 v15, v15
	v_rcp_f32_e32 v16, v16
	s_nop 0
	v_mul_f32_e32 v8, v8, v7
	v_mul_f32_e32 v9, v9, v17
	v_mul_f32_e32 v10, v10, v18
	v_mul_f32_e32 v11, v11, v12
	v_mul_f32_e32 v19, v19, v13
	v_mul_f32_e32 v20, v20, v14
	v_mul_f32_e32 v21, v21, v15
	v_mul_f32_e32 v22, v22, v16
	v_add_u32_e32 v6, 0xb0, v6
	v_med3_f32 v7, v8, s35, v24
	v_med3_f32 v9, v9, s35, v24
	v_mov_b32_e32 v8, v195
	v_med3_f32 v12, v19, s35, v24
	v_med3_f32 v13, v20, s35, v24
	v_cvt_pk_fp8_f32 v8, v7, v9
	v_mov_b32_e32 v9, v195
	v_cvt_pk_fp8_f32 v9, v12, v13
	v_med3_f32 v10, v10, s35, v24
	v_med3_f32 v11, v11, s35, v24
	v_med3_f32 v7, v21, s35, v24
	v_med3_f32 v12, v22, s35, v24
	v_cvt_pk_fp8_f32 v8, v10, v11 op_sel:[0,0,1]
	v_cvt_pk_fp8_f32 v9, v7, v12 op_sel:[0,0,1]
	v_mad_i64_i32 v[4:5], s[0:1], v6, s4, v[4:5]
	v_lshl_add_u64 v[2:3], v[4:5], 0, v[2:3]
	s_mov_b64 s[0:1], -1
	global_store_dwordx2 v[2:3], v[8:9], off
	s_cbranch_vccnz .LBB0_952
	s_andn2_b64 vcc, exec, s[10:11]
	s_cbranch_vccnz .LBB0_951
	s_mov_b32 s101, 1
	s_branch .LBB0_951

.LBB0_1046:
	s_mov_b32 s55, 22
	s_cmp_lt_i32 s55, 1
	s_cbranch_scc1 .LBB0_1054
	v_mov_b32_e32 v236, 0xf149f2ca
	v_mov_b32_e32 v252, 0x7f800000
	v_mov_b32_e32 v1, -1
	v_mov_b32_e32 v193, 0x260
	v_mov_b64_e32 v[246:247], 0x200
	v_mov_b32_e32 v192, 0x358637bd
	s_mov_b32 s56, 2
	s_mov_b64 s[20:21], 0x58080
	s_cmp_lg_u32 s101, 0
	s_cbranch_scc0 .Lrob_7
	s_barrier
	s_mov_b32 s101, 0

.LBB0_1051:
	v_mov_b32_e32 v66, v0
	s_mov_b64 s[4:5], 0x40000
	v_ashrrev_i32_e32 v67, 2, v66
	v_and_b32_e32 v67, 0xffffffc0, v67
	v_lshl_add_u32 v67, s53, 8, v67
	v_and_or_b32 v138, v66, 15, v67
	v_lshrrev_b32_e32 v66, 1, v66
	v_ashrrev_i32_e32 v139, 31, v138
	v_and_b32_e32 v66, 0x78, v66
	v_lshl_add_u64 v[136:137], v[138:139], 2, s[10:11]
	v_lshl_or_b32 v140, s54, 8, v66
	global_load_dword v146, v[136:137], off
	global_load_dword v147, v[136:137], off offset:64
	global_load_dword v148, v[136:137], off offset:128
	global_load_dword v149, v[136:137], off offset:192
	global_load_dword v150, v[136:137], off offset:512
	global_load_dword v151, v[136:137], off offset:576
	global_load_dword v152, v[136:137], off offset:640
	global_load_dword v153, v[136:137], off offset:704
	v_ashrrev_i32_e32 v141, 31, v140
	v_lshlrev_b64 v[144:145], 11, v[138:139]
	s_waitcnt vmcnt(0)
	v_mul_f32_e32 v142, 0x3b800000, v146
	v_pk_mul_f32 v[68:69], v[128:129], v[142:143] op_sel_hi:[1,0]
	v_pk_mul_f32 v[66:67], v[126:127], v[142:143] op_sel_hi:[1,0]
	v_pk_mul_f32 v[124:125], v[124:125], v[142:143] op_sel_hi:[1,0]
	v_pk_mul_f32 v[122:123], v[122:123], v[142:143] op_sel_hi:[1,0]
	v_cvt_pk_bf16_f32 v66, v66, v67
	v_cvt_pk_bf16_f32 v67, v68, v69
	v_pk_mul_f32 v[116:117], v[116:117], v[142:143] op_sel_hi:[1,0]
	v_cvt_pk_bf16_f32 v68, v122, v123
	v_cvt_pk_bf16_f32 v69, v124, v125
	v_lshl_add_u64 v[122:123], s[12:13], 0, v[144:145]
	v_lshlrev_b64 v[124:125], 1, v[140:141]
	v_lshl_add_u64 v[122:123], v[122:123], 0, v[124:125]
	global_store_dwordx4 v[122:123], v[66:69], off
	v_pk_mul_f32 v[114:115], v[114:115], v[142:143] op_sel_hi:[1,0]
	s_nop 0
	v_pk_mul_f32 v[66:67], v[118:119], v[142:143] op_sel_hi:[1,0]
	v_pk_mul_f32 v[68:69], v[120:121], v[142:143] op_sel_hi:[1,0]
	v_cvt_pk_bf16_f32 v66, v66, v67
	s_nop 0
	v_cvt_pk_bf16_f32 v67, v68, v69
	v_cvt_pk_bf16_f32 v68, v114, v115
	v_cvt_pk_bf16_f32 v69, v116, v117
	global_store_dwordx4 v[122:123], v[66:69], off offset:256
	s_nop 1
	v_or_b32_e32 v66, 16, v138
	v_ashrrev_i32_e32 v67, 31, v66
	v_lshlrev_b64 v[116:117], 11, v[66:67]
	s_nop 1
	v_mul_f32_e32 v114, 0x3b800000, v147
	v_pk_mul_f32 v[68:69], v[112:113], v[114:115] op_sel_hi:[1,0]
	v_pk_mul_f32 v[66:67], v[110:111], v[114:115] op_sel_hi:[1,0]
	v_pk_mul_f32 v[106:107], v[106:107], v[114:115] op_sel_hi:[1,0]
	v_cvt_pk_bf16_f32 v66, v66, v67
	v_cvt_pk_bf16_f32 v67, v68, v69
	v_pk_mul_f32 v[108:109], v[108:109], v[114:115] op_sel_hi:[1,0]
	v_cvt_pk_bf16_f32 v68, v106, v107
	v_lshl_add_u64 v[106:107], s[12:13], 0, v[116:117]
	v_lshl_add_u64 v[106:107], v[106:107], 0, v[124:125]
	v_cvt_pk_bf16_f32 v69, v108, v109
	global_store_dwordx4 v[106:107], v[66:69], off
	v_pk_mul_f32 v[100:101], v[100:101], v[114:115] op_sel_hi:[1,0]
	v_pk_mul_f32 v[98:99], v[98:99], v[114:115] op_sel_hi:[1,0]
	v_pk_mul_f32 v[66:67], v[102:103], v[114:115] op_sel_hi:[1,0]
	v_pk_mul_f32 v[68:69], v[104:105], v[114:115] op_sel_hi:[1,0]
	v_cvt_pk_bf16_f32 v66, v66, v67
	s_nop 0
	v_cvt_pk_bf16_f32 v67, v68, v69
	v_cvt_pk_bf16_f32 v68, v98, v99
	v_cvt_pk_bf16_f32 v69, v100, v101
	global_store_dwordx4 v[106:107], v[66:69], off offset:256
	s_nop 1
	v_or_b32_e32 v66, 32, v138
	v_ashrrev_i32_e32 v67, 31, v66
	v_lshlrev_b64 v[100:101], 11, v[66:67]
	s_nop 1
	v_mul_f32_e32 v98, 0x3b800000, v148
	v_pk_mul_f32 v[68:69], v[96:97], v[98:99] op_sel_hi:[1,0]
	v_pk_mul_f32 v[66:67], v[94:95], v[98:99] op_sel_hi:[1,0]
	v_pk_mul_f32 v[90:91], v[90:91], v[98:99] op_sel_hi:[1,0]
	v_cvt_pk_bf16_f32 v66, v66, v67
	v_cvt_pk_bf16_f32 v67, v68, v69
	v_pk_mul_f32 v[92:93], v[92:93], v[98:99] op_sel_hi:[1,0]
	v_cvt_pk_bf16_f32 v68, v90, v91
	v_lshl_add_u64 v[90:91], s[12:13], 0, v[100:101]
	v_lshl_add_u64 v[90:91], v[90:91], 0, v[124:125]
	v_cvt_pk_bf16_f32 v69, v92, v93
	global_store_dwordx4 v[90:91], v[66:69], off
	v_pk_mul_f32 v[84:85], v[84:85], v[98:99] op_sel_hi:[1,0]
	v_pk_mul_f32 v[82:83], v[82:83], v[98:99] op_sel_hi:[1,0]
	v_pk_mul_f32 v[66:67], v[86:87], v[98:99] op_sel_hi:[1,0]
	v_pk_mul_f32 v[68:69], v[88:89], v[98:99] op_sel_hi:[1,0]
	v_cvt_pk_bf16_f32 v66, v66, v67
	s_nop 0
	v_cvt_pk_bf16_f32 v67, v68, v69
	v_cvt_pk_bf16_f32 v68, v82, v83
	v_cvt_pk_bf16_f32 v69, v84, v85
	global_store_dwordx4 v[90:91], v[66:69], off offset:256
	s_nop 1
	v_or_b32_e32 v66, 48, v138
	v_ashrrev_i32_e32 v67, 31, v66
	v_lshlrev_b64 v[84:85], 11, v[66:67]
	s_nop 1
	v_mul_f32_e32 v82, 0x3b800000, v149
	v_pk_mul_f32 v[68:69], v[80:81], v[82:83] op_sel_hi:[1,0]
	v_pk_mul_f32 v[66:67], v[78:79], v[82:83] op_sel_hi:[1,0]
	v_pk_mul_f32 v[74:75], v[74:75], v[82:83] op_sel_hi:[1,0]
	v_cvt_pk_bf16_f32 v66, v66, v67
	v_cvt_pk_bf16_f32 v67, v68, v69
	v_pk_mul_f32 v[76:77], v[76:77], v[82:83] op_sel_hi:[1,0]
	v_cvt_pk_bf16_f32 v68, v74, v75
	v_lshl_add_u64 v[74:75], s[12:13], 0, v[84:85]
	v_cvt_pk_bf16_f32 v69, v76, v77
	v_lshl_add_u64 v[74:75], v[74:75], 0, v[124:125]
	global_store_dwordx4 v[74:75], v[66:69], off
	s_nop 1
	v_pk_mul_f32 v[68:69], v[70:71], v[82:83] op_sel_hi:[1,0]
	v_pk_mul_f32 v[70:71], v[12:13], v[82:83] op_sel_hi:[1,0]
	v_pk_mul_f32 v[12:13], v[10:11], v[82:83] op_sel_hi:[1,0]
	v_pk_mul_f32 v[66:67], v[72:73], v[82:83] op_sel_hi:[1,0]
	v_cvt_pk_bf16_f32 v10, v68, v69
	s_nop 0
	v_cvt_pk_bf16_f32 v11, v66, v67
	v_cvt_pk_bf16_f32 v12, v12, v13
	v_cvt_pk_bf16_f32 v13, v70, v71
	global_store_dwordx4 v[74:75], v[10:13], off offset:256
	s_nop 1
	v_mul_f32_e32 v66, 0x3b800000, v150
	v_pk_mul_f32 v[12:13], v[64:65], v[66:67] op_sel_hi:[1,0]
	v_pk_mul_f32 v[10:11], v[62:63], v[66:67] op_sel_hi:[1,0]
	v_pk_mul_f32 v[60:61], v[60:61], v[66:67] op_sel_hi:[1,0]
	v_pk_mul_f32 v[58:59], v[58:59], v[66:67] op_sel_hi:[1,0]
	v_cvt_pk_bf16_f32 v10, v10, v11
	v_cvt_pk_bf16_f32 v11, v12, v13
	v_pk_mul_f32 v[52:53], v[52:53], v[66:67] op_sel_hi:[1,0]
	v_cvt_pk_bf16_f32 v12, v58, v59
	v_cvt_pk_bf16_f32 v13, v60, v61
	v_add_co_u32_e32 v60, vcc, s88, v122
	v_lshl_add_u64 v[58:59], v[122:123], 0, s[4:5]
	s_nop 0
	v_addc_co_u32_e32 v61, vcc, 0, v123, vcc
	global_store_dwordx4 v[60:61], v[10:13], off
	v_pk_mul_f32 v[50:51], v[50:51], v[66:67] op_sel_hi:[1,0]
	s_mov_b64 s[4:5], 0x48000
	v_pk_mul_f32 v[12:13], v[56:57], v[66:67] op_sel_hi:[1,0]
	v_pk_mul_f32 v[10:11], v[54:55], v[66:67] op_sel_hi:[1,0]
	s_nop 0
	v_cvt_pk_bf16_f32 v10, v10, v11
	v_cvt_pk_bf16_f32 v11, v12, v13
	v_cvt_pk_bf16_f32 v12, v50, v51
	v_cvt_pk_bf16_f32 v13, v52, v53
	global_store_dwordx4 v[58:59], v[10:13], off offset:256
	s_nop 1
	v_mul_f32_e32 v50, 0x3b800000, v151
	v_pk_mul_f32 v[12:13], v[48:49], v[50:51] op_sel_hi:[1,0]
	v_pk_mul_f32 v[10:11], v[46:47], v[50:51] op_sel_hi:[1,0]
	v_pk_mul_f32 v[44:45], v[44:45], v[50:51] op_sel_hi:[1,0]
	v_pk_mul_f32 v[42:43], v[42:43], v[50:51] op_sel_hi:[1,0]
	v_cvt_pk_bf16_f32 v10, v10, v11
	v_cvt_pk_bf16_f32 v11, v12, v13
	v_pk_mul_f32 v[36:37], v[36:37], v[50:51] op_sel_hi:[1,0]
	v_cvt_pk_bf16_f32 v12, v42, v43
	v_cvt_pk_bf16_f32 v13, v44, v45
	v_add_co_u32_e32 v44, vcc, s94, v122
	v_lshl_add_u64 v[42:43], v[122:123], 0, s[4:5]
	s_nop 0
	v_addc_co_u32_e32 v45, vcc, 0, v123, vcc
	global_store_dwordx4 v[44:45], v[10:13], off
	v_pk_mul_f32 v[34:35], v[34:35], v[50:51] op_sel_hi:[1,0]
	s_mov_b64 s[4:5], 0x50000
	v_pk_mul_f32 v[12:13], v[40:41], v[50:51] op_sel_hi:[1,0]
	v_pk_mul_f32 v[10:11], v[38:39], v[50:51] op_sel_hi:[1,0]
	s_nop 0
	v_cvt_pk_bf16_f32 v10, v10, v11
	v_cvt_pk_bf16_f32 v11, v12, v13
	v_cvt_pk_bf16_f32 v12, v34, v35
	v_cvt_pk_bf16_f32 v13, v36, v37
	global_store_dwordx4 v[42:43], v[10:13], off offset:256
	s_nop 1
	v_mul_f32_e32 v34, 0x3b800000, v152
	v_pk_mul_f32 v[12:13], v[32:33], v[34:35] op_sel_hi:[1,0]
	v_pk_mul_f32 v[10:11], v[30:31], v[34:35] op_sel_hi:[1,0]
	v_pk_mul_f32 v[28:29], v[28:29], v[34:35] op_sel_hi:[1,0]
	v_pk_mul_f32 v[26:27], v[26:27], v[34:35] op_sel_hi:[1,0]
	v_cvt_pk_bf16_f32 v10, v10, v11
	v_cvt_pk_bf16_f32 v11, v12, v13
	v_pk_mul_f32 v[20:21], v[20:21], v[34:35] op_sel_hi:[1,0]
	v_cvt_pk_bf16_f32 v12, v26, v27
	v_cvt_pk_bf16_f32 v13, v28, v29
	v_add_co_u32_e32 v28, vcc, s89, v122
	v_lshl_add_u64 v[26:27], v[122:123], 0, s[4:5]
	s_nop 0
	v_addc_co_u32_e32 v29, vcc, 0, v123, vcc
	global_store_dwordx4 v[28:29], v[10:13], off
	v_pk_mul_f32 v[18:19], v[18:19], v[34:35] op_sel_hi:[1,0]
	s_mov_b64 s[4:5], 0x58000
	v_pk_mul_f32 v[12:13], v[24:25], v[34:35] op_sel_hi:[1,0]
	v_pk_mul_f32 v[10:11], v[22:23], v[34:35] op_sel_hi:[1,0]
	s_nop 0
	v_cvt_pk_bf16_f32 v10, v10, v11
	v_cvt_pk_bf16_f32 v11, v12, v13
	v_cvt_pk_bf16_f32 v12, v18, v19
	v_cvt_pk_bf16_f32 v13, v20, v21
	global_store_dwordx4 v[26:27], v[10:13], off offset:256
	s_nop 1
	v_mul_f32_e32 v18, 0x3b800000, v153
	v_pk_mul_f32 v[12:13], v[16:17], v[18:19] op_sel_hi:[1,0]
	v_pk_mul_f32 v[10:11], v[14:15], v[18:19] op_sel_hi:[1,0]
	v_pk_mul_f32 v[16:17], v[228:229], v[18:19] op_sel_hi:[1,0]
	v_cvt_pk_bf16_f32 v10, v10, v11
	v_cvt_pk_bf16_f32 v11, v12, v13
	v_pk_mul_f32 v[14:15], v[230:231], v[18:19] op_sel_hi:[1,0]
	v_cvt_pk_bf16_f32 v12, v16, v17
	v_add_co_u32_e32 v16, vcc, s95, v122
	v_cvt_pk_bf16_f32 v13, v14, v15
	v_lshl_add_u64 v[14:15], v[122:123], 0, s[4:5]
	s_nop 0
	v_addc_co_u32_e32 v17, vcc, 0, v123, vcc
	global_store_dwordx4 v[16:17], v[10:13], off
	s_mov_b64 s[4:5], -1
	s_and_b64 vcc, exec, s[2:3]
	v_pk_mul_f32 v[10:11], v[4:5], v[18:19] op_sel_hi:[1,0]
	v_pk_mul_f32 v[4:5], v[2:3], v[18:19] op_sel_hi:[1,0]
	v_pk_mul_f32 v[8:9], v[8:9], v[18:19] op_sel_hi:[1,0]
	v_pk_mul_f32 v[6:7], v[6:7], v[18:19] op_sel_hi:[1,0]
	s_nop 0
	v_cvt_pk_bf16_f32 v2, v6, v7
	v_cvt_pk_bf16_f32 v3, v8, v9
	v_cvt_pk_bf16_f32 v4, v4, v5
	v_cvt_pk_bf16_f32 v5, v10, v11
	global_store_dwordx4 v[14:15], v[2:5], off offset:256
	s_cbranch_vccnz .LBB0_1035
	s_andn2_b64 vcc, exec, s[8:9]
	s_cbranch_vccnz .LBB0_1034
	s_mov_b32 s101, 1
	s_branch .LBB0_1034
